# baseline (speedup 1.0000x reference)
_Z13lstm_ta_fusedPKfPKDv8_DF16_S0_S0_S3_S0_PfP15HIP_vector_typeIjLj2EE:
	s_load_dwordx8 s[12:19], s[0:1], 0x0
	v_readfirstlane_b32 s35, v0
	s_lshr_b32 s28, s35, 6
	s_mul_i32 s4, s28, 0x6000
	s_mul_hi_u32 s3, s28, 0x6000
	s_waitcnt lgkmcnt(0)
	s_add_u32 s14, s14, s4
	v_bfe_u32 v1, v0, 2, 4
	s_addc_u32 s15, s15, s3
	s_lshl_b32 s33, s28, 4
	v_and_b32_e32 v204, 12, v1
	v_or_b32_e32 v2, s33, v204
	v_lshlrev_b32_e32 v2, 2, v2
	global_load_dwordx4 v[100:103], v2, s[16:17]
	global_load_dwordx4 v[108:111], v2, s[16:17] offset:512
	global_load_dwordx4 v[222:225], v2, s[18:19]
	global_load_dwordx4 v[130:133], v2, s[18:19] offset:512
	global_load_dwordx4 v[134:137], v2, s[16:17] offset:1024
	global_load_dwordx4 v[146:149], v2, s[16:17] offset:1536
	global_load_dwordx4 v[150:153], v2, s[18:19] offset:1024
	global_load_dwordx4 v[154:157], v2, s[18:19] offset:1536
	s_load_dwordx8 s[4:11], s[0:1], 0x20
	v_and_b32_e32 v170, 63, v0
	v_mov_b32_e32 v187, 0
	v_lshlrev_b32_e32 v186, 4, v170
	s_movk_i32 s3, 0x1000
	v_lshl_add_u64 v[22:23], s[14:15], 0, v[186:187]
	v_add_co_u32_e32 v24, vcc, s3, v22
	s_movk_i32 s17, 0x2000
	s_nop 0
	v_addc_co_u32_e32 v25, vcc, 0, v23, vcc
	v_add_co_u32_e32 v26, vcc, s17, v22
	s_lshl_b32 s34, s2, 4
	s_and_b32 s21, s13, 0xffff
	s_waitcnt lgkmcnt(0)
	s_and_b32 s17, s5, 0xffff
	s_mul_hi_u32 s0, s2, 0x32000
	s_mul_i32 s2, s2, 0x32000
	s_movk_i32 s36, 0x3000
	v_addc_co_u32_e32 v27, vcc, 0, v23, vcc
	s_add_u32 s2, s10, s2
	v_add_co_u32_e32 v30, vcc, s36, v22
	s_addc_u32 s3, s11, s0
	s_ashr_i32 s0, s34, 31
	s_movk_i32 s16, 0x4000
	v_addc_co_u32_e32 v31, vcc, 0, v23, vcc
	v_or_b32_e32 v164, s34, v1
	v_mov_b32_e32 v165, s0
	s_mov_b32 s29, 0
	v_add_co_u32_e32 v28, vcc, s16, v22
	v_lshlrev_b32_e32 v1, 1, v0
	s_movk_i32 s18, 0x5000
	v_addc_co_u32_e32 v29, vcc, 0, v23, vcc
	s_lshl_b32 s0, s28, 5
	s_mov_b32 s1, s29
	v_add_co_u32_e32 v94, vcc, s18, v22
	v_addc_co_u32_e32 v95, vcc, 0, v23, vcc
	s_add_u32 s84, s14, 0x1000
	s_addc_u32 s85, s15, 0
	s_add_u32 s86, s14, 0x2000
	s_addc_u32 s87, s15, 0
	s_add_u32 s88, s14, 0x3000
	s_addc_u32 s89, s15, 0
	s_add_u32 s90, s14, 0x4000
	s_addc_u32 s91, s15, 0
	s_add_u32 s92, s14, 0x5000
	s_addc_u32 s93, s15, 0
	s_lshl_b32 s94, s28, 11
	s_add_u32 s94, s4, s94
	s_addc_u32 s95, s5, 0
	s_lshl_b32 s40, s28, 5
	s_cmp_gt_u32 s35, 0xff
	s_cselect_b32 s41, 0x800, 0
	s_sub_i32 s42, 0x800, s41
	v_lshlrev_b32_e32 v210, 8, v164
	v_and_b32_e32 v211, 3, v0
	v_lshl_add_u32 v210, v211, 3, v210
	v_add_u32_e32 v210, s40, v210
	v_add_u32_e32 v211, 0x100000, v210
	v_add_u32_e32 v212, 0x200000, v210
	v_add_u32_e32 v213, 0x300000, v210
	v_add_u32_e32 v214, 0x400000, v210
	v_add_u32_e32 v215, 0x500000, v210
	v_add_u32_e32 v216, s41, v186
	v_add_u32_e32 v217, s42, v186
	v_add_u32_e32 v218, 0x4000, v186
	v_add_u32_e32 v219, 0x8000, v186
	s_nop 0
	global_load_dwordx2 v[166:167], v210, s[12:13]
	global_load_dwordx2 v[168:169], v211, s[12:13]
	global_load_dwordx2 v[196:197], v212, s[12:13]
	global_load_dwordx2 v[194:195], v213, s[12:13]
	global_load_dwordx2 v[192:193], v214, s[12:13]
	global_load_dwordx2 v[190:191], v215, s[12:13]
	global_load_dwordx4 v[70:73], v186, s[84:85]
	global_load_dwordx4 v[66:69], v186, s[84:85] offset:1024
	global_load_dwordx4 v[74:77], v186, s[86:87] offset:2048
	global_load_dwordx4 v[78:81], v186, s[86:87] offset:3072
	global_load_dwordx4 v[82:85], v186, s[90:91]
	global_load_dwordx4 v[86:89], v186, s[90:91] offset:1024
	global_load_dwordx4 v[90:93], v186, s[92:93] offset:2048
	global_load_dwordx4 v[94:97], v186, s[92:93] offset:3072
	global_load_dwordx4 v[138:141], v186, s[94:95]
	global_load_dwordx4 v[142:145], v186, s[94:95] offset:1024
	global_load_dwordx4 v[122:125], v218, s[94:95]
	global_load_dwordx4 v[126:129], v218, s[94:95] offset:1024
	global_load_dwordx4 v[114:117], v219, s[94:95]
	global_load_dwordx4 v[118:121], v219, s[94:95] offset:1024
	global_load_dwordx4 v[54:57], v216, s[14:15]
	global_load_dwordx4 v[58:61], v216, s[14:15] offset:1024
	global_load_dwordx4 v[62:65], v217, s[14:15]
	global_load_dwordx4 v[50:53], v217, s[14:15] offset:1024
	global_load_dwordx4 v[34:37], v216, s[84:85] offset:2048
	global_load_dwordx4 v[38:41], v216, s[84:85] offset:3072
	global_load_dwordx4 v[42:45], v217, s[84:85] offset:2048
	global_load_dwordx4 v[46:49], v217, s[84:85] offset:3072
	global_load_dwordx4 v[18:21], v216, s[88:89]
	global_load_dwordx4 v[14:17], v216, s[88:89] offset:1024
	global_load_dwordx4 v[10:13], v217, s[88:89]
	global_load_dwordx4 v[26:29], v217, s[88:89] offset:1024
	global_load_dwordx4 v[2:5], v216, s[90:91] offset:2048
	global_load_dwordx4 v[6:9], v216, s[90:91] offset:3072
	global_load_dwordx4 v[22:25], v217, s[90:91] offset:2048
	global_load_dwordx4 v[30:33], v217, s[90:91] offset:3072
	s_and_b32 s25, s3, 0xffff
	v_lshlrev_b32_e32 v188, 3, v0
	s_mov_b32 s10, 0xc038aa3b
	v_and_b32_e32 v205, 15, v0
	s_mov_b32 s11, 0xbfb8aa3b
	s_mov_b32 s23, 0x20000
	v_lshl_or_b32 v189, s28, 11, v186
	s_mov_b32 s22, 0x3200000
	s_mov_b32 s20, s12
	s_mov_b32 s18, 0xc8000
	s_mov_b32 s19, s23
	s_mov_b32 s26, 0x32000
	s_mov_b32 s24, s2
	s_mov_b32 s27, s23
	v_or_b32_e32 v208, 0x400, v189
	s_mov_b32 s37, 0x18000
	s_mov_b32 s38, 0xf149f2ca
	v_mov_b32_e32 v202, 0x42a00000
	v_mov_b32_e32 v200, v187
	v_mov_b32_e32 v201, v187
	v_mov_b32_e32 v198, v187
	v_mov_b32_e32 v199, v187
	s_waitcnt vmcnt(43)
	v_mov_b32_e32 v104, v100
	s_waitcnt vmcnt(42)
	v_mov_b32_e32 v105, v108
	v_mov_b32_e32 v108, v101
	v_lshlrev_b64 v[100:101], 8, v[164:165]
	s_waitcnt vmcnt(39)
	v_mov_b32_e32 v160, v136
	v_lshl_add_u64 v[100:101], s[12:13], 0, v[100:101]
	v_and_b32_e32 v136, 6, v1
	v_mov_b32_e32 v112, v134
	s_waitcnt vmcnt(38)
	v_mov_b32_e32 v113, v146
	v_mov_b32_e32 v146, v135
	v_mov_b32_e32 v134, v102
	v_mov_b32_e32 v135, v110
	v_mov_b32_e32 v110, v103
	v_lshl_add_u64 v[100:101], v[100:101], 0, s[0:1]
	v_lshlrev_b32_e32 v102, 2, v136
	v_mov_b32_e32 v103, v187
	v_lshl_add_u64 v[100:101], v[100:101], 0, v[102:103]
	s_mov_b32 s0, 0x100000
	v_add_co_u32_e32 v102, vcc, s0, v100
	s_mov_b32 s0, 0x200000
	s_nop 0
	v_addc_co_u32_e32 v103, vcc, 0, v101, vcc
	v_mov_b32_e32 v106, v222
	v_mov_b32_e32 v107, v130
	v_mov_b32_e32 v130, v223
	s_nop 0
	s_nop 0
	s_nop 0
	v_add_co_u32_e32 v102, vcc, s0, v100
	s_mov_b32 s0, 0x300000
	s_nop 0
	v_addc_co_u32_e32 v103, vcc, 0, v101, vcc
	s_mov_b32 s0, 0x400000
	s_nop 0
	v_add_co_u32_e32 v102, vcc, s0, v100
	s_mov_b32 s0, 0x500000
	s_nop 0
	v_addc_co_u32_e32 v103, vcc, 0, v101, vcc
	v_add_co_u32_e32 v100, vcc, s0, v100
	s_lshl_b64 s[0:1], s[28:29], 11
	s_add_u32 s0, s4, s0
	v_addc_co_u32_e32 v101, vcc, 0, v101, vcc
	s_addc_u32 s1, s5, s1
	v_lshl_add_u64 v[100:101], s[0:1], 0, v[186:187]
	v_add_co_u32_e32 v102, vcc, s16, v100
	v_addc_co_u32_e32 v103, vcc, 0, v101, vcc
	s_mov_b32 s0, 0x8000
	v_add_co_u32_e32 v100, vcc, s0, v100
	v_addc_co_u32_e32 v101, vcc, 0, v101, vcc
	v_pk_add_f32 v[102:103], v[108:109], v[130:131]
	v_lshlrev_b32_e32 v130, 6, v164
	v_lshl_add_u32 v130, s28, 3, v130
	v_lshlrev_b32_e32 v1, 2, v170
	v_or_b32_e32 v130, v130, v136
	v_lshl_or_b32 v1, s28, 8, v1
	v_lshlrev_b32_e32 v209, 2, v130
	s_waitcnt vmcnt(37)
	v_mov_b32_e32 v158, v150
	s_waitcnt vmcnt(36)
	v_mov_b32_e32 v159, v154
	v_mov_b32_e32 v154, v151
	v_mov_b32_e32 v150, v224
	v_mov_b32_e32 v151, v132
	v_mov_b32_e32 v161, v148
	v_mov_b32_e32 v163, v156
	v_mov_b32_e32 v148, v137
	v_mov_b32_e32 v156, v153
	v_mov_b32_e32 v162, v152
	v_mov_b32_e32 v132, v225
	v_pk_add_f32 v[98:99], v[104:105], v[106:107]
	v_pk_add_f32 v[100:101], v[112:113], v[158:159]
	v_pk_add_f32 v[104:105], v[146:147], v[154:155]
	v_pk_add_f32 v[106:107], v[134:135], v[150:151]
	v_pk_add_f32 v[112:113], v[148:149], v[156:157]
	v_pk_add_f32 v[110:111], v[110:111], v[132:133]
	v_lshrrev_b32_e32 v132, 1, v0
	v_and_b32_e32 v132, 8, v132
	s_mov_b32 s0, s11
	v_pk_add_f32 v[108:109], v[160:161], v[162:163]
	s_cmpk_gt_u32 s35, 0xff
	v_pk_mul_f32 v[100:101], v[100:101], s[10:11]
	v_pk_mul_f32 v[98:99], v[98:99], s[0:1] op_sel_hi:[1,0]
	v_pk_mul_f32 v[104:105], v[104:105], s[10:11]
	v_pk_mul_f32 v[102:103], v[102:103], s[0:1] op_sel_hi:[1,0]
	v_pk_mul_f32 v[108:109], v[108:109], s[10:11]
	v_pk_mul_f32 v[106:107], v[106:107], s[0:1] op_sel_hi:[1,0]
	v_pk_mul_f32 v[112:113], v[112:113], s[10:11]
	v_pk_mul_f32 v[110:111], v[110:111], s[0:1] op_sel_hi:[1,0]
	s_mov_b32 s16, s4
	s_mov_b32 s13, 3
	s_cselect_b64 s[4:5], -1, 0
	v_mov_b32_e32 v146, v187
	s_waitcnt vmcnt(35)
	v_cvt_pk_f16_f32 v130, v166, v167
	s_waitcnt vmcnt(34)
	v_cvt_pk_f16_f32 v131, v168, v169
	ds_write2st64_b32 v1, v130, v131 offset1:8
	v_mov_b32_e32 v130, v187
	v_mov_b32_e32 v131, v187
	ds_write_b64 v188, v[130:131] offset:12288
	s_waitcnt lgkmcnt(0)
	s_barrier
	ds_read_b128 v[150:153], v186
	ds_read_b128 v[154:157], v186 offset:1024
	v_bfe_u32 v130, v0, 5, 1
	v_lshl_or_b32 v207, s28, 1, v130
	v_lshlrev_b32_e32 v130, 8, v207
	v_lshlrev_b32_e32 v131, 4, v205
	v_or3_b32 v206, v130, v131, v132
	v_mov_b32_e32 v147, v187
	v_mov_b32_e32 v148, v187
	v_mov_b32_e32 v149, v187
	s_mov_b32 s28, 0x900000
	s_mov_b32 s12, 0x4038aa3b
	s_waitcnt vmcnt(21) lgkmcnt(0)
	v_mov_b64_e32 v[130:131], v[138:139]
	s_waitcnt vmcnt(20)
	v_mov_b64_e32 v[134:135], v[142:143]
	v_mov_b64_e32 v[132:133], v[140:141]
	v_mov_b64_e32 v[136:137], v[144:145]
	s_mov_b32 s40, 0
	s_mov_b32 s41, 0xbeb17218
	s_mov_b32 s42, 0x42a00000
	s_mov_b32 s44, 0
	s_mov_b32 s45, 0x500000
	s_mov_b32 s46, 0x8000
	s_cmp_gt_u32 s35, 0xff
	s_cselect_b32 s47, 0x800, 0
	v_add_u32_e32 v252, 0x2000, v186
	v_subrev_u32_e32 v253, s47, v252
	v_add_u32_e32 v252, s47, v252
	v_add_u32_e32 v248, 0x1000, v252
	v_add_u32_e32 v249, 0x1000, v253
	s_mov_b32 s64, s6
	s_and_b32 s65, s7, 0xffff
	s_movk_i32 s66, 0xc8
	s_mov_b32 s67, 0x20000
	v_and_b32_e32 v254, 31, v0
	v_lshlrev_b32_e32 v254, 2, v254
	buffer_load_dword v255, v254, s[64:67], 0 offen offset:128
	buffer_load_dword v254, v254, s[64:67], 0 offen
	v_mfma_f32_16x16x32_f16 v[210:213], v[70:73], v[150:153], v[98:101]
	v_mfma_f32_16x16x32_f16 v[214:217], v[74:77], v[150:153], v[102:105]
	v_mfma_f32_16x16x32_f16 v[210:213], v[66:69], v[154:157], v[210:213]
	v_mfma_f32_16x16x32_f16 v[214:217], v[78:81], v[154:157], v[214:217]
	s_add_u32 s48, s20, 0x600000
	s_addc_u32 s49, s21, 0
	s_sub_u32 s50, s22, 0x600000
	s_mov_b32 s51, s23
	s_add_u32 s68, s16, 0xc000
	s_addc_u32 s69, s17, 0
	s_sub_u32 s70, s18, 0xc000
	s_mov_b32 s71, s19
	s_add_u32 s52, s20, 0x700000
	s_addc_u32 s53, s21, 0
	s_sub_u32 s54, s22, 0x700000
	s_mov_b32 s55, s23
	s_add_u32 s72, s16, 0x10000
	s_addc_u32 s73, s17, 0
	s_sub_u32 s74, s18, 0x10000
	s_mov_b32 s75, s19
	s_add_u32 s56, s20, 0x800000
	s_addc_u32 s57, s21, 0
	s_sub_u32 s58, s22, 0x800000
	s_mov_b32 s59, s23
	s_add_u32 s76, s16, 0x14000
	s_addc_u32 s77, s17, 0
	s_sub_u32 s78, s18, 0x14000
	s_mov_b32 s79, s19
	s_add_u32 s60, s20, 0x900000
	s_addc_u32 s61, s21, 0
	s_sub_u32 s62, s22, 0x900000
	s_mov_b32 s63, s23
	s_add_u32 s80, s16, 0x18000
	s_addc_u32 s81, s17, 0
	s_sub_u32 s82, s18, 0x18000
	s_mov_b32 s83, s19
	v_mfma_f32_16x16x32_f16 v[218:221], v[82:85], v[150:153], v[106:109]
	v_mfma_f32_16x16x32_f16 v[222:225], v[90:93], v[150:153], v[110:113]
	v_mfma_f32_16x16x32_f16 v[218:221], v[86:89], v[154:157], v[218:221]
	v_mfma_f32_16x16x32_f16 v[222:225], v[94:97], v[154:157], v[222:225]
	s_waitcnt lgkmcnt(2)
	s_waitcnt lgkmcnt(0)
	s_nop 0
	v_cvt_pk_f16_f32 v251, v196, v197
	ds_write_b32 v1, v251 offset:4096
	ds_read_b128 v[150:153], v186 offset:2048
	ds_read_b128 v[154:157], v186 offset:3072
	s_add_i32 s45, s45, 0x100000
	s_add_i32 s46, s46, 0x4000
	s_movk_i32 s47, 0x0
	s_add_i32 s43, s40, -12
	s_lshl_b32 s43, s43, 12
	s_cmp_lt_u32 s40, 14
	s_cselect_b32 s43, s47, s43
	v_exp_f32_e32 v226, v210
	v_exp_f32_e32 v227, v211
	v_min_f32_e32 v228, s42, v212
	v_exp_f32_e32 v229, v213
	v_exp_f32_e32 v228, v228
	v_add_f32_e32 v227, 1.0, v227
	v_fma_f32 v230, v228, s41, s41
	v_rcp_f32_e32 v227, v227
	v_fma_f32 v230, v226, v230, v230
	v_rcp_f32_e32 v230, v230
	s_nop 0
	v_fma_f32 v226, -v228, v230, v230
	v_fma_f32 v200, v200, v227, v226
	v_exp_f32_e32 v226, v200
	s_nop 0
	v_add_f32_e32 v227, 1.0, v226
	v_fma_f32 v227, v229, v227, v227
	v_rcp_f32_e32 v227, v227
	s_nop 0
	v_fma_f32 v226, -v226, v227, v227
	v_exp_f32_e32 v231, v214
	v_exp_f32_e32 v232, v215
	v_min_f32_e32 v233, s42, v216
	v_exp_f32_e32 v234, v217
	v_exp_f32_e32 v233, v233
	v_exp_f32_e32 v236, v218
	v_add_f32_e32 v232, 1.0, v232
	v_fma_f32 v235, v233, s41, s41
	v_exp_f32_e32 v227, v219
	v_rcp_f32_e32 v232, v232
	v_fma_f32 v235, v231, v235, v235
	v_min_f32_e32 v228, s42, v220
	v_rcp_f32_e32 v235, v235
	s_nop 0
	v_fma_f32 v231, -v233, v235, v235
	v_exp_f32_e32 v229, v221
	v_fma_f32 v201, v201, v232, v231
	v_exp_f32_e32 v231, v201
	v_exp_f32_e32 v228, v228
	v_add_f32_e32 v232, 1.0, v231
	v_fma_f32 v232, v234, v232, v232
	v_add_f32_e32 v227, 1.0, v227
	v_rcp_f32_e32 v232, v232
	s_nop 0
	v_fma_f32 v231, -v231, v232, v232
	v_fma_f32 v230, v228, s41, s41
	v_cvt_pk_f16_f32 v246, v226, v231
	v_exp_f32_e32 v231, v222
	v_rcp_f32_e32 v227, v227
	v_exp_f32_e32 v232, v223
	buffer_load_dwordx4 v[138:141], v189, s[16:19], s46 offen
	buffer_load_dwordx4 v[142:145], v208, s[16:19], s46 offen
	v_min_f32_e32 v233, s42, v224
	v_fma_f32 v230, v236, v230, v230
	v_exp_f32_e32 v234, v225
	s_waitcnt lgkmcnt(0)
	v_mfma_f32_16x16x32_f16 v[210:213], v[70:73], v[150:153], v[98:101]
	v_exp_f32_e32 v233, v233
	v_rcp_f32_e32 v230, v230
	v_add_f32_e32 v232, 1.0, v232
	v_mfma_f32_16x16x32_f16 v[214:217], v[74:77], v[150:153], v[102:105]
	v_fma_f32 v235, v233, s41, s41
	v_fma_f32 v236, -v228, v230, v230
	v_rcp_f32_e32 v232, v232
	v_fma_f32 v235, v231, v235, v235
	v_fma_f32 v198, v198, v227, v236
	v_rcp_f32_e32 v235, v235
	s_nop 0
	v_fma_f32 v231, -v233, v235, v235
	v_exp_f32_e32 v236, v198
	v_fma_f32 v199, v199, v232, v231
	v_exp_f32_e32 v231, v199
	v_add_f32_e32 v227, 1.0, v236
	v_add_f32_e32 v232, 1.0, v231
	v_fma_f32 v232, v234, v232, v232
	v_fma_f32 v227, v229, v227, v227
	v_rcp_f32_e32 v232, v232
	s_nop 0
	v_fma_f32 v231, -v231, v232, v232
	v_rcp_f32_e32 v227, v227
	s_nop 0
	v_fma_f32 v236, -v236, v227, v227
	v_cvt_pk_f16_f32 v247, v236, v231
	ds_write_b64 v206, v[246:247] offset:8192
	v_mfma_f32_16x16x32_f16 v[210:213], v[66:69], v[154:157], v[210:213]
	v_mfma_f32_16x16x32_f16 v[214:217], v[78:81], v[154:157], v[214:217]
	v_mov_b32_e32 v174, v246
	v_mov_b32_e32 v175, v247
	buffer_load_dwordx2 v[196:197], v209, s[20:23], s45 offen
	s_add_i32 s40, s40, 1
	s_add_i32 s44, s44, 0x1000
	s_waitcnt lgkmcnt(0)
	s_barrier
	ds_read_b128 v[158:161], v252 offset:0
	ds_read_b128 v[162:165], v252 offset:1024
	ds_read_b128 v[166:169], v253 offset:2048
	ds_read_b128 v[170:173], v253 offset:3072
	v_mfma_f32_16x16x32_f16 v[218:221], v[82:85], v[150:153], v[106:109]
	v_mfma_f32_16x16x32_f16 v[222:225], v[90:93], v[150:153], v[110:113]
	v_mfma_f32_16x16x32_f16 v[218:221], v[86:89], v[154:157], v[218:221]
	v_mfma_f32_16x16x32_f16 v[222:225], v[94:97], v[154:157], v[222:225]
	s_waitcnt vmcnt(5) lgkmcnt(2)
	v_mfma_f32_16x16x32_f16 v[210:213], v[54:57], v[158:161], v[210:213]
	v_mfma_f32_16x16x32_f16 v[210:213], v[58:61], v[162:165], v[210:213]
	s_waitcnt lgkmcnt(0)
	v_mfma_f32_16x16x32_f16 v[210:213], v[62:65], v[166:169], v[210:213]
	v_mfma_f32_16x16x32_f16 v[210:213], v[50:53], v[170:173], v[210:213]
	s_waitcnt vmcnt(9)
	v_cvt_pk_f16_f32 v251, v194, v195
	ds_write_b32 v1, v251 offset:6144
	ds_read_b128 v[150:153], v186 offset:4096
	ds_read_b128 v[154:157], v186 offset:5120
	s_add_i32 s45, s45, 0x100000
	s_add_i32 s46, s46, 0x4000
	s_movk_i32 s47, 0x1000
	s_add_i32 s43, s40, -12
	s_lshl_b32 s43, s43, 12
	s_cmp_lt_u32 s40, 14
	s_cselect_b32 s43, s47, s43
	v_exp_f32_e32 v226, v210
	v_exp_f32_e32 v227, v211
	v_mfma_f32_16x16x32_f16 v[214:217], v[34:37], v[158:161], v[214:217]
	v_min_f32_e32 v228, s42, v212
	v_exp_f32_e32 v229, v213
	v_mfma_f32_16x16x32_f16 v[214:217], v[38:41], v[162:165], v[214:217]
	v_exp_f32_e32 v228, v228
	v_add_f32_e32 v227, 1.0, v227
	v_mfma_f32_16x16x32_f16 v[214:217], v[42:45], v[166:169], v[214:217]
	v_fma_f32 v230, v228, s41, s41
	v_rcp_f32_e32 v227, v227
	v_mfma_f32_16x16x32_f16 v[214:217], v[46:49], v[170:173], v[214:217]
	v_fma_f32 v230, v226, v230, v230
	v_rcp_f32_e32 v230, v230
	v_mfma_f32_16x16x32_f16 v[218:221], v[18:21], v[158:161], v[218:221]
	v_fma_f32 v226, -v228, v230, v230
	v_fma_f32 v200, v200, v227, v226
	v_mfma_f32_16x16x32_f16 v[218:221], v[14:17], v[162:165], v[218:221]
	v_exp_f32_e32 v226, v200
	s_nop 0
	v_add_f32_e32 v227, 1.0, v226
	v_mfma_f32_16x16x32_f16 v[218:221], v[10:13], v[166:169], v[218:221]
	v_fma_f32 v227, v229, v227, v227
	v_rcp_f32_e32 v227, v227
	v_mfma_f32_16x16x32_f16 v[218:221], v[26:29], v[170:173], v[218:221]
	v_fma_f32 v226, -v226, v227, v227
	v_exp_f32_e32 v231, v214
	v_mfma_f32_16x16x32_f16 v[222:225], v[2:5], v[158:161], v[222:225]
	v_exp_f32_e32 v232, v215
	v_min_f32_e32 v233, s42, v216
	v_mfma_f32_16x16x32_f16 v[222:225], v[6:9], v[162:165], v[222:225]
	v_exp_f32_e32 v234, v217
	v_exp_f32_e32 v233, v233
	v_mfma_f32_16x16x32_f16 v[222:225], v[22:25], v[166:169], v[222:225]
	v_exp_f32_e32 v236, v218
	v_add_f32_e32 v232, 1.0, v232
	v_mfma_f32_16x16x32_f16 v[222:225], v[30:33], v[170:173], v[222:225]
	v_fma_f32 v235, v233, s41, s41
	v_exp_f32_e32 v227, v219
	v_rcp_f32_e32 v232, v232
	v_fma_f32 v235, v231, v235, v235
	v_min_f32_e32 v228, s42, v220
	v_rcp_f32_e32 v235, v235
	s_nop 0
	v_fma_f32 v231, -v233, v235, v235
	v_exp_f32_e32 v229, v221
	v_fma_f32 v201, v201, v232, v231
	v_exp_f32_e32 v231, v201
	v_exp_f32_e32 v228, v228
	v_add_f32_e32 v232, 1.0, v231
	v_fma_f32 v232, v234, v232, v232
	v_add_f32_e32 v227, 1.0, v227
	v_rcp_f32_e32 v232, v232
	v_mfma_f32_16x16x32_f16 v[146:149], v[130:133], v[158:161], v[146:149]
	v_fma_f32 v231, -v231, v232, v232
	v_fma_f32 v230, v228, s41, s41
	v_cvt_pk_f16_f32 v246, v226, v231
	v_mfma_f32_16x16x32_f16 v[146:149], v[134:137], v[162:165], v[146:149]
	v_exp_f32_e32 v231, v222
	v_rcp_f32_e32 v227, v227
	v_exp_f32_e32 v232, v223
	buffer_load_dwordx4 v[130:133], v189, s[16:19], s46 offen
	buffer_load_dwordx4 v[134:137], v208, s[16:19], s46 offen
	v_min_f32_e32 v233, s42, v224
	v_fma_f32 v230, v236, v230, v230
	v_exp_f32_e32 v234, v225
	s_waitcnt lgkmcnt(0)
	v_mfma_f32_16x16x32_f16 v[210:213], v[70:73], v[150:153], v[98:101]
	v_exp_f32_e32 v233, v233
	v_rcp_f32_e32 v230, v230
	v_add_f32_e32 v232, 1.0, v232
	v_mfma_f32_16x16x32_f16 v[214:217], v[74:77], v[150:153], v[102:105]
	v_fma_f32 v235, v233, s41, s41
	v_fma_f32 v236, -v228, v230, v230
	v_rcp_f32_e32 v232, v232
	v_fma_f32 v235, v231, v235, v235
	v_fma_f32 v198, v198, v227, v236
	v_rcp_f32_e32 v235, v235
	s_nop 0
	v_fma_f32 v231, -v233, v235, v235
	v_exp_f32_e32 v236, v198
	v_fma_f32 v199, v199, v232, v231
	v_exp_f32_e32 v231, v199
	v_add_f32_e32 v227, 1.0, v236
	v_add_f32_e32 v232, 1.0, v231
	v_fma_f32 v232, v234, v232, v232
	v_fma_f32 v227, v229, v227, v227
	v_rcp_f32_e32 v232, v232
	s_nop 0
	v_fma_f32 v231, -v231, v232, v232
	v_rcp_f32_e32 v227, v227
	s_nop 0
	v_fma_f32 v236, -v236, v227, v227
	v_cvt_pk_f16_f32 v247, v236, v231
	ds_write_b64 v206, v[246:247] offset:12288
	v_mfma_f32_16x16x32_f16 v[210:213], v[66:69], v[154:157], v[210:213]
	v_mfma_f32_16x16x32_f16 v[214:217], v[78:81], v[154:157], v[214:217]
	v_mov_b32_e32 v176, v246
	v_mov_b32_e32 v177, v247
	buffer_load_dwordx2 v[194:195], v209, s[20:23], s45 offen
	s_add_i32 s40, s40, 1
	s_add_i32 s44, s44, 0x1000
	s_waitcnt lgkmcnt(0)
	s_barrier
	ds_read_b128 v[158:161], v252 offset:4096
	ds_read_b128 v[162:165], v252 offset:5120
	ds_read_b128 v[166:169], v253 offset:6144
	ds_read_b128 v[170:173], v253 offset:7168
	v_mfma_f32_16x16x32_f16 v[218:221], v[82:85], v[150:153], v[106:109]
	v_mfma_f32_16x16x32_f16 v[222:225], v[90:93], v[150:153], v[110:113]
	v_mfma_f32_16x16x32_f16 v[218:221], v[86:89], v[154:157], v[218:221]
	v_mfma_f32_16x16x32_f16 v[222:225], v[94:97], v[154:157], v[222:225]
	s_waitcnt lgkmcnt(2)
	v_mfma_f32_16x16x32_f16 v[210:213], v[54:57], v[158:161], v[210:213]
	v_mfma_f32_16x16x32_f16 v[210:213], v[58:61], v[162:165], v[210:213]
	s_waitcnt lgkmcnt(0)
	v_mfma_f32_16x16x32_f16 v[210:213], v[62:65], v[166:169], v[210:213]
	v_mfma_f32_16x16x32_f16 v[210:213], v[50:53], v[170:173], v[210:213]
	s_waitcnt vmcnt(9)
	v_cvt_pk_f16_f32 v251, v192, v193
	ds_write_b32 v1, v251 offset:0
	ds_read_b128 v[150:153], v186 offset:6144
	ds_read_b128 v[154:157], v186 offset:7168
	s_add_i32 s45, s45, 0x100000
	s_add_i32 s46, s46, 0x4000
	s_movk_i32 s47, 0x0
	s_add_i32 s43, s40, -12
	s_lshl_b32 s43, s43, 12
	s_cmp_lt_u32 s40, 14
	s_cselect_b32 s43, s47, s43
	v_exp_f32_e32 v226, v210
	v_exp_f32_e32 v227, v211
	v_mfma_f32_16x16x32_f16 v[214:217], v[34:37], v[158:161], v[214:217]
	v_min_f32_e32 v228, s42, v212
	v_exp_f32_e32 v229, v213
	v_mfma_f32_16x16x32_f16 v[214:217], v[38:41], v[162:165], v[214:217]
	v_exp_f32_e32 v228, v228
	v_add_f32_e32 v227, 1.0, v227
	v_mfma_f32_16x16x32_f16 v[214:217], v[42:45], v[166:169], v[214:217]
	v_fma_f32 v230, v228, s41, s41
	v_rcp_f32_e32 v227, v227
	v_mfma_f32_16x16x32_f16 v[214:217], v[46:49], v[170:173], v[214:217]
	v_fma_f32 v230, v226, v230, v230
	v_rcp_f32_e32 v230, v230
	v_mfma_f32_16x16x32_f16 v[218:221], v[18:21], v[158:161], v[218:221]
	v_fma_f32 v226, -v228, v230, v230
	v_fma_f32 v200, v200, v227, v226
	v_mfma_f32_16x16x32_f16 v[218:221], v[14:17], v[162:165], v[218:221]
	v_exp_f32_e32 v226, v200
	s_nop 0
	v_add_f32_e32 v227, 1.0, v226
	v_mfma_f32_16x16x32_f16 v[218:221], v[10:13], v[166:169], v[218:221]
	v_fma_f32 v227, v229, v227, v227
	v_rcp_f32_e32 v227, v227
	v_mfma_f32_16x16x32_f16 v[218:221], v[26:29], v[170:173], v[218:221]
	v_fma_f32 v226, -v226, v227, v227
	v_exp_f32_e32 v231, v214
	v_mfma_f32_16x16x32_f16 v[222:225], v[2:5], v[158:161], v[222:225]
	v_exp_f32_e32 v232, v215
	v_min_f32_e32 v233, s42, v216
	v_mfma_f32_16x16x32_f16 v[222:225], v[6:9], v[162:165], v[222:225]
	v_exp_f32_e32 v234, v217
	v_exp_f32_e32 v233, v233
	v_mfma_f32_16x16x32_f16 v[222:225], v[22:25], v[166:169], v[222:225]
	v_exp_f32_e32 v236, v218
	v_add_f32_e32 v232, 1.0, v232
	v_mfma_f32_16x16x32_f16 v[222:225], v[30:33], v[170:173], v[222:225]
	v_fma_f32 v235, v233, s41, s41
	v_exp_f32_e32 v227, v219
	v_rcp_f32_e32 v232, v232
	v_fma_f32 v235, v231, v235, v235
	v_min_f32_e32 v228, s42, v220
	v_rcp_f32_e32 v235, v235
	s_nop 0
	v_fma_f32 v231, -v233, v235, v235
	v_exp_f32_e32 v229, v221
	v_fma_f32 v201, v201, v232, v231
	v_exp_f32_e32 v231, v201
	v_exp_f32_e32 v228, v228
	v_add_f32_e32 v232, 1.0, v231
	v_fma_f32 v232, v234, v232, v232
	v_add_f32_e32 v227, 1.0, v227
	v_rcp_f32_e32 v232, v232
	v_mfma_f32_16x16x32_f16 v[146:149], v[122:125], v[158:161], v[146:149]
	v_fma_f32 v231, -v231, v232, v232
	v_fma_f32 v230, v228, s41, s41
	v_cvt_pk_f16_f32 v246, v226, v231
	v_mfma_f32_16x16x32_f16 v[146:149], v[126:129], v[162:165], v[146:149]
	v_exp_f32_e32 v231, v222
	v_rcp_f32_e32 v227, v227
	v_exp_f32_e32 v232, v223
	buffer_load_dwordx4 v[122:125], v189, s[16:19], s46 offen
	buffer_load_dwordx4 v[126:129], v208, s[16:19], s46 offen
	v_min_f32_e32 v233, s42, v224
	v_fma_f32 v230, v236, v230, v230
	v_exp_f32_e32 v234, v225
	s_waitcnt lgkmcnt(0)
	v_mfma_f32_16x16x32_f16 v[210:213], v[70:73], v[150:153], v[98:101]
	v_exp_f32_e32 v233, v233
	v_rcp_f32_e32 v230, v230
	v_add_f32_e32 v232, 1.0, v232
	v_mfma_f32_16x16x32_f16 v[214:217], v[74:77], v[150:153], v[102:105]
	v_fma_f32 v235, v233, s41, s41
	v_fma_f32 v236, -v228, v230, v230
	v_rcp_f32_e32 v232, v232
	v_fma_f32 v235, v231, v235, v235
	v_fma_f32 v198, v198, v227, v236
	v_rcp_f32_e32 v235, v235
	s_nop 0
	v_fma_f32 v231, -v233, v235, v235
	v_exp_f32_e32 v236, v198
	v_fma_f32 v199, v199, v232, v231
	v_exp_f32_e32 v231, v199
	v_add_f32_e32 v227, 1.0, v236
	v_add_f32_e32 v232, 1.0, v231
	v_fma_f32 v232, v234, v232, v232
	v_fma_f32 v227, v229, v227, v227
	v_rcp_f32_e32 v232, v232
	s_nop 0
	v_fma_f32 v231, -v231, v232, v232
	v_rcp_f32_e32 v227, v227
	s_nop 0
	v_fma_f32 v236, -v236, v227, v227
	v_cvt_pk_f16_f32 v247, v236, v231
	ds_write_b64 v206, v[246:247] offset:8192
	v_mfma_f32_16x16x32_f16 v[210:213], v[66:69], v[154:157], v[210:213]
	v_mfma_f32_16x16x32_f16 v[214:217], v[78:81], v[154:157], v[214:217]
	v_mov_b32_e32 v178, v246
	v_mov_b32_e32 v179, v247
	buffer_load_dwordx2 v[192:193], v209, s[20:23], s45 offen
	s_add_i32 s40, s40, 1
	s_add_i32 s44, s44, 0x1000
	s_waitcnt lgkmcnt(0)
	s_barrier
	ds_read_b128 v[158:161], v252 offset:0
	ds_read_b128 v[162:165], v252 offset:1024
	ds_read_b128 v[166:169], v253 offset:2048
	ds_read_b128 v[170:173], v253 offset:3072
	v_mfma_f32_16x16x32_f16 v[218:221], v[82:85], v[150:153], v[106:109]
	v_mfma_f32_16x16x32_f16 v[222:225], v[90:93], v[150:153], v[110:113]
	v_mfma_f32_16x16x32_f16 v[218:221], v[86:89], v[154:157], v[218:221]
	v_mfma_f32_16x16x32_f16 v[222:225], v[94:97], v[154:157], v[222:225]
	s_waitcnt lgkmcnt(2)
	v_mfma_f32_16x16x32_f16 v[210:213], v[54:57], v[158:161], v[210:213]
	v_mfma_f32_16x16x32_f16 v[210:213], v[58:61], v[162:165], v[210:213]
	s_waitcnt lgkmcnt(0)
	v_mfma_f32_16x16x32_f16 v[210:213], v[62:65], v[166:169], v[210:213]
	v_mfma_f32_16x16x32_f16 v[210:213], v[50:53], v[170:173], v[210:213]
	s_waitcnt vmcnt(9)
	v_cvt_pk_f16_f32 v251, v190, v191
	ds_write_b32 v1, v251 offset:2048
	ds_read_b128 v[150:153], v186 offset:0
	ds_read_b128 v[154:157], v186 offset:1024
	s_add_i32 s45, s45, 0x100000
	s_add_i32 s46, s46, 0x4000
	s_movk_i32 s47, 0x1000
	s_add_i32 s43, s40, -12
	s_lshl_b32 s43, s43, 12
	s_cmp_lt_u32 s40, 14
	s_cselect_b32 s43, s47, s43
	v_exp_f32_e32 v226, v210
	v_exp_f32_e32 v227, v211
	v_mfma_f32_16x16x32_f16 v[214:217], v[34:37], v[158:161], v[214:217]
	v_min_f32_e32 v228, s42, v212
	v_exp_f32_e32 v229, v213
	v_mfma_f32_16x16x32_f16 v[214:217], v[38:41], v[162:165], v[214:217]
	v_exp_f32_e32 v228, v228
	v_add_f32_e32 v227, 1.0, v227
	v_mfma_f32_16x16x32_f16 v[214:217], v[42:45], v[166:169], v[214:217]
	v_fma_f32 v230, v228, s41, s41
	v_rcp_f32_e32 v227, v227
	v_mfma_f32_16x16x32_f16 v[214:217], v[46:49], v[170:173], v[214:217]
	v_fma_f32 v230, v226, v230, v230
	v_rcp_f32_e32 v230, v230
	v_mfma_f32_16x16x32_f16 v[218:221], v[18:21], v[158:161], v[218:221]
	v_fma_f32 v226, -v228, v230, v230
	v_fma_f32 v200, v200, v227, v226
	v_mfma_f32_16x16x32_f16 v[218:221], v[14:17], v[162:165], v[218:221]
	v_exp_f32_e32 v226, v200
	s_nop 0
	v_add_f32_e32 v227, 1.0, v226
	v_mfma_f32_16x16x32_f16 v[218:221], v[10:13], v[166:169], v[218:221]
	v_fma_f32 v227, v229, v227, v227
	v_rcp_f32_e32 v227, v227
	v_mfma_f32_16x16x32_f16 v[218:221], v[26:29], v[170:173], v[218:221]
	v_fma_f32 v226, -v226, v227, v227
	v_exp_f32_e32 v231, v214
	v_mfma_f32_16x16x32_f16 v[222:225], v[2:5], v[158:161], v[222:225]
	v_exp_f32_e32 v232, v215
	v_min_f32_e32 v233, s42, v216
	v_mfma_f32_16x16x32_f16 v[222:225], v[6:9], v[162:165], v[222:225]
	v_exp_f32_e32 v234, v217
	v_exp_f32_e32 v233, v233
	v_mfma_f32_16x16x32_f16 v[222:225], v[22:25], v[166:169], v[222:225]
	v_exp_f32_e32 v236, v218
	v_add_f32_e32 v232, 1.0, v232
	v_mfma_f32_16x16x32_f16 v[222:225], v[30:33], v[170:173], v[222:225]
	v_fma_f32 v235, v233, s41, s41
	v_exp_f32_e32 v227, v219
	v_rcp_f32_e32 v232, v232
	v_fma_f32 v235, v231, v235, v235
	v_min_f32_e32 v228, s42, v220
	v_rcp_f32_e32 v235, v235
	s_nop 0
	v_fma_f32 v231, -v233, v235, v235
	v_exp_f32_e32 v229, v221
	v_fma_f32 v201, v201, v232, v231
	v_exp_f32_e32 v231, v201
	v_exp_f32_e32 v228, v228
	v_add_f32_e32 v232, 1.0, v231
	v_fma_f32 v232, v234, v232, v232
	v_add_f32_e32 v227, 1.0, v227
	v_rcp_f32_e32 v232, v232
	v_mfma_f32_16x16x32_f16 v[146:149], v[114:117], v[158:161], v[146:149]
	v_fma_f32 v231, -v231, v232, v232
	v_fma_f32 v230, v228, s41, s41
	v_cvt_pk_f16_f32 v246, v226, v231
	v_mfma_f32_16x16x32_f16 v[146:149], v[118:121], v[162:165], v[146:149]
	v_exp_f32_e32 v231, v222
	v_rcp_f32_e32 v227, v227
	v_exp_f32_e32 v232, v223
	buffer_load_dwordx4 v[114:117], v189, s[16:19], s46 offen
	buffer_load_dwordx4 v[118:121], v208, s[16:19], s46 offen
	v_min_f32_e32 v233, s42, v224
	v_fma_f32 v230, v236, v230, v230
	v_exp_f32_e32 v234, v225
	s_waitcnt lgkmcnt(0)
	v_mfma_f32_16x16x32_f16 v[210:213], v[70:73], v[150:153], v[98:101]
	v_exp_f32_e32 v233, v233
	v_rcp_f32_e32 v230, v230
	v_add_f32_e32 v232, 1.0, v232
	v_mfma_f32_16x16x32_f16 v[214:217], v[74:77], v[150:153], v[102:105]
	v_fma_f32 v235, v233, s41, s41
	v_fma_f32 v236, -v228, v230, v230
	v_rcp_f32_e32 v232, v232
	v_fma_f32 v235, v231, v235, v235
	v_fma_f32 v198, v198, v227, v236
	v_rcp_f32_e32 v235, v235
	s_nop 0
	v_fma_f32 v231, -v233, v235, v235
	v_exp_f32_e32 v236, v198
	v_fma_f32 v199, v199, v232, v231
	v_exp_f32_e32 v231, v199
	v_add_f32_e32 v227, 1.0, v236
	v_add_f32_e32 v232, 1.0, v231
	v_fma_f32 v232, v234, v232, v232
	v_fma_f32 v227, v229, v227, v227
	v_rcp_f32_e32 v232, v232
	s_nop 0
	v_fma_f32 v231, -v231, v232, v232
	v_rcp_f32_e32 v227, v227
	s_nop 0
	v_fma_f32 v236, -v236, v227, v227
	v_cvt_pk_f16_f32 v247, v236, v231
	ds_write_b64 v206, v[246:247] offset:12288
	v_mfma_f32_16x16x32_f16 v[210:213], v[66:69], v[154:157], v[210:213]
	v_mfma_f32_16x16x32_f16 v[214:217], v[78:81], v[154:157], v[214:217]
	v_mov_b32_e32 v180, v246
	v_mov_b32_e32 v181, v247
	buffer_load_dwordx2 v[190:191], v209, s[20:23], s45 offen
	s_add_i32 s40, s40, 1
	s_add_i32 s44, s44, 0x1000
	s_waitcnt lgkmcnt(0)
	s_barrier
	ds_read_b128 v[158:161], v252 offset:4096
	ds_read_b128 v[162:165], v252 offset:5120
	ds_read_b128 v[166:169], v253 offset:6144
	ds_read_b128 v[170:173], v253 offset:7168
	v_mfma_f32_16x16x32_f16 v[218:221], v[82:85], v[150:153], v[106:109]
	v_mfma_f32_16x16x32_f16 v[222:225], v[90:93], v[150:153], v[110:113]
	v_mfma_f32_16x16x32_f16 v[218:221], v[86:89], v[154:157], v[218:221]
	v_mfma_f32_16x16x32_f16 v[222:225], v[94:97], v[154:157], v[222:225]
	s_waitcnt lgkmcnt(2)
	v_mfma_f32_16x16x32_f16 v[210:213], v[54:57], v[158:161], v[210:213]
	v_mfma_f32_16x16x32_f16 v[210:213], v[58:61], v[162:165], v[210:213]
	s_waitcnt lgkmcnt(0)
	v_mfma_f32_16x16x32_f16 v[210:213], v[62:65], v[166:169], v[210:213]
	v_mfma_f32_16x16x32_f16 v[210:213], v[50:53], v[170:173], v[210:213]
	s_waitcnt vmcnt(9)
	v_cvt_pk_f16_f32 v251, v196, v197
	ds_write_b32 v1, v251 offset:4096
	ds_read_b128 v[150:153], v186 offset:2048
	ds_read_b128 v[154:157], v186 offset:3072
	s_add_i32 s45, s45, 0x100000
	s_add_i32 s46, s46, 0x4000
	s_movk_i32 s47, 0x0
	s_add_i32 s43, s40, -12
	s_lshl_b32 s43, s43, 12
	s_cmp_lt_u32 s40, 14
	s_cselect_b32 s43, s47, s43
	v_exp_f32_e32 v226, v210
	v_exp_f32_e32 v227, v211
	v_mfma_f32_16x16x32_f16 v[214:217], v[34:37], v[158:161], v[214:217]
	v_min_f32_e32 v228, s42, v212
	v_exp_f32_e32 v229, v213
	v_mfma_f32_16x16x32_f16 v[214:217], v[38:41], v[162:165], v[214:217]
	v_exp_f32_e32 v228, v228
	v_add_f32_e32 v227, 1.0, v227
	v_mfma_f32_16x16x32_f16 v[214:217], v[42:45], v[166:169], v[214:217]
	v_fma_f32 v230, v228, s41, s41
	v_rcp_f32_e32 v227, v227
	v_mfma_f32_16x16x32_f16 v[214:217], v[46:49], v[170:173], v[214:217]
	v_fma_f32 v230, v226, v230, v230
	v_rcp_f32_e32 v230, v230
	v_mfma_f32_16x16x32_f16 v[218:221], v[18:21], v[158:161], v[218:221]
	v_fma_f32 v226, -v228, v230, v230
	v_fma_f32 v200, v200, v227, v226
	v_mfma_f32_16x16x32_f16 v[218:221], v[14:17], v[162:165], v[218:221]
	v_exp_f32_e32 v226, v200
	s_nop 0
	v_add_f32_e32 v227, 1.0, v226
	v_mfma_f32_16x16x32_f16 v[218:221], v[10:13], v[166:169], v[218:221]
	v_fma_f32 v227, v229, v227, v227
	v_rcp_f32_e32 v227, v227
	v_mfma_f32_16x16x32_f16 v[218:221], v[26:29], v[170:173], v[218:221]
	v_fma_f32 v226, -v226, v227, v227
	v_exp_f32_e32 v231, v214
	v_mfma_f32_16x16x32_f16 v[222:225], v[2:5], v[158:161], v[222:225]
	v_exp_f32_e32 v232, v215
	v_min_f32_e32 v233, s42, v216
	v_mfma_f32_16x16x32_f16 v[222:225], v[6:9], v[162:165], v[222:225]
	v_exp_f32_e32 v234, v217
	v_exp_f32_e32 v233, v233
	v_mfma_f32_16x16x32_f16 v[222:225], v[22:25], v[166:169], v[222:225]
	v_exp_f32_e32 v236, v218
	v_add_f32_e32 v232, 1.0, v232
	v_mfma_f32_16x16x32_f16 v[222:225], v[30:33], v[170:173], v[222:225]
	v_fma_f32 v235, v233, s41, s41
	v_exp_f32_e32 v227, v219
	v_rcp_f32_e32 v232, v232
	v_fma_f32 v235, v231, v235, v235
	v_min_f32_e32 v228, s42, v220
	v_rcp_f32_e32 v235, v235
	s_nop 0
	v_fma_f32 v231, -v233, v235, v235
	v_exp_f32_e32 v229, v221
	v_fma_f32 v201, v201, v232, v231
	v_exp_f32_e32 v231, v201
	v_exp_f32_e32 v228, v228
	v_add_f32_e32 v232, 1.0, v231
	v_fma_f32 v232, v234, v232, v232
	v_add_f32_e32 v227, 1.0, v227
	v_rcp_f32_e32 v232, v232
	v_mfma_f32_16x16x32_f16 v[146:149], v[138:141], v[158:161], v[146:149]
	v_fma_f32 v231, -v231, v232, v232
	v_fma_f32 v230, v228, s41, s41
	v_cvt_pk_f16_f32 v246, v226, v231
	v_mfma_f32_16x16x32_f16 v[146:149], v[142:145], v[162:165], v[146:149]
	v_exp_f32_e32 v231, v222
	v_rcp_f32_e32 v227, v227
	v_exp_f32_e32 v232, v223
	buffer_load_dwordx4 v[138:141], v189, s[16:19], s46 offen
	buffer_load_dwordx4 v[142:145], v208, s[16:19], s46 offen
	v_min_f32_e32 v233, s42, v224
	v_fma_f32 v230, v236, v230, v230
	v_exp_f32_e32 v234, v225
	s_waitcnt lgkmcnt(0)
	v_mfma_f32_16x16x32_f16 v[210:213], v[70:73], v[150:153], v[98:101]
	v_exp_f32_e32 v233, v233
	v_rcp_f32_e32 v230, v230
	v_add_f32_e32 v232, 1.0, v232
	v_mfma_f32_16x16x32_f16 v[214:217], v[74:77], v[150:153], v[102:105]
	v_fma_f32 v235, v233, s41, s41
	v_fma_f32 v236, -v228, v230, v230
	v_rcp_f32_e32 v232, v232
	v_fma_f32 v235, v231, v235, v235
	v_fma_f32 v198, v198, v227, v236
	v_rcp_f32_e32 v235, v235
	s_nop 0
	v_fma_f32 v231, -v233, v235, v235
	v_exp_f32_e32 v236, v198
	v_fma_f32 v199, v199, v232, v231
	v_exp_f32_e32 v231, v199
	v_add_f32_e32 v227, 1.0, v236
	v_add_f32_e32 v232, 1.0, v231
	v_fma_f32 v232, v234, v232, v232
	v_fma_f32 v227, v229, v227, v227
	v_rcp_f32_e32 v232, v232
	s_nop 0
	v_fma_f32 v231, -v231, v232, v232
	v_rcp_f32_e32 v227, v227
	s_nop 0
	v_fma_f32 v236, -v236, v227, v227
	v_cvt_pk_f16_f32 v247, v236, v231
	ds_write_b64 v206, v[246:247] offset:8192
	v_mfma_f32_16x16x32_f16 v[210:213], v[66:69], v[154:157], v[210:213]
	v_mfma_f32_16x16x32_f16 v[214:217], v[78:81], v[154:157], v[214:217]
	v_mov_b32_e32 v182, v246
	v_mov_b32_e32 v183, v247
	buffer_load_dwordx2 v[196:197], v209, s[20:23], s45 offen
	s_add_i32 s40, s40, 1
	s_add_i32 s44, s44, 0x1000
	s_waitcnt lgkmcnt(0)
	s_barrier
	ds_read_b128 v[158:161], v252 offset:0
	ds_read_b128 v[162:165], v252 offset:1024
	ds_read_b128 v[166:169], v253 offset:2048
	ds_read_b128 v[170:173], v253 offset:3072
	v_mfma_f32_16x16x32_f16 v[218:221], v[82:85], v[150:153], v[106:109]
	v_mfma_f32_16x16x32_f16 v[222:225], v[90:93], v[150:153], v[110:113]
	v_mfma_f32_16x16x32_f16 v[218:221], v[86:89], v[154:157], v[218:221]
	v_mfma_f32_16x16x32_f16 v[222:225], v[94:97], v[154:157], v[222:225]
	s_waitcnt lgkmcnt(2)
	v_mfma_f32_16x16x32_f16 v[210:213], v[54:57], v[158:161], v[210:213]
	v_mfma_f32_16x16x32_f16 v[210:213], v[58:61], v[162:165], v[210:213]
	s_waitcnt lgkmcnt(0)
	v_mfma_f32_16x16x32_f16 v[210:213], v[62:65], v[166:169], v[210:213]
	v_mfma_f32_16x16x32_f16 v[210:213], v[50:53], v[170:173], v[210:213]
	s_waitcnt vmcnt(9)
	v_cvt_pk_f16_f32 v251, v194, v195
	ds_write_b32 v1, v251 offset:6144
	ds_read_b128 v[150:153], v186 offset:4096
	ds_read_b128 v[154:157], v186 offset:5120
	s_add_i32 s45, s45, 0x100000
	s_add_i32 s46, s46, 0x4000
	s_movk_i32 s47, 0x1000
	s_add_i32 s43, s40, -12
	s_lshl_b32 s43, s43, 12
	s_cmp_lt_u32 s40, 14
	s_cselect_b32 s43, s47, s43
	v_exp_f32_e32 v226, v210
	v_exp_f32_e32 v227, v211
	v_mfma_f32_16x16x32_f16 v[214:217], v[34:37], v[158:161], v[214:217]
	v_min_f32_e32 v228, s42, v212
	v_exp_f32_e32 v229, v213
	v_mfma_f32_16x16x32_f16 v[214:217], v[38:41], v[162:165], v[214:217]
	v_exp_f32_e32 v228, v228
	v_add_f32_e32 v227, 1.0, v227
	v_mfma_f32_16x16x32_f16 v[214:217], v[42:45], v[166:169], v[214:217]
	v_fma_f32 v230, v228, s41, s41
	v_rcp_f32_e32 v227, v227
	v_mfma_f32_16x16x32_f16 v[214:217], v[46:49], v[170:173], v[214:217]
	v_fma_f32 v230, v226, v230, v230
	v_rcp_f32_e32 v230, v230
	v_mfma_f32_16x16x32_f16 v[218:221], v[18:21], v[158:161], v[218:221]
	v_fma_f32 v226, -v228, v230, v230
	v_fma_f32 v200, v200, v227, v226
	v_mfma_f32_16x16x32_f16 v[218:221], v[14:17], v[162:165], v[218:221]
	v_exp_f32_e32 v226, v200
	s_nop 0
	v_add_f32_e32 v227, 1.0, v226
	v_mfma_f32_16x16x32_f16 v[218:221], v[10:13], v[166:169], v[218:221]
	v_fma_f32 v227, v229, v227, v227
	v_rcp_f32_e32 v227, v227
	v_mfma_f32_16x16x32_f16 v[218:221], v[26:29], v[170:173], v[218:221]
	v_fma_f32 v226, -v226, v227, v227
	v_exp_f32_e32 v231, v214
	v_mfma_f32_16x16x32_f16 v[222:225], v[2:5], v[158:161], v[222:225]
	v_exp_f32_e32 v232, v215
	v_min_f32_e32 v233, s42, v216
	v_mfma_f32_16x16x32_f16 v[222:225], v[6:9], v[162:165], v[222:225]
	v_exp_f32_e32 v234, v217
	v_exp_f32_e32 v233, v233
	v_mfma_f32_16x16x32_f16 v[222:225], v[22:25], v[166:169], v[222:225]
	v_exp_f32_e32 v236, v218
	v_add_f32_e32 v232, 1.0, v232
	v_mfma_f32_16x16x32_f16 v[222:225], v[30:33], v[170:173], v[222:225]
	v_fma_f32 v235, v233, s41, s41
	v_exp_f32_e32 v227, v219
	v_rcp_f32_e32 v232, v232
	v_fma_f32 v235, v231, v235, v235
	v_min_f32_e32 v228, s42, v220
	v_rcp_f32_e32 v235, v235
	s_nop 0
	v_fma_f32 v231, -v233, v235, v235
	v_exp_f32_e32 v229, v221
	v_fma_f32 v201, v201, v232, v231
	v_exp_f32_e32 v231, v201
	v_exp_f32_e32 v228, v228
	v_add_f32_e32 v232, 1.0, v231
	v_fma_f32 v232, v234, v232, v232
	v_add_f32_e32 v227, 1.0, v227
	v_rcp_f32_e32 v232, v232
	v_mfma_f32_16x16x32_f16 v[146:149], v[130:133], v[158:161], v[146:149]
	v_fma_f32 v231, -v231, v232, v232
	v_fma_f32 v230, v228, s41, s41
	v_cvt_pk_f16_f32 v246, v226, v231
	v_mfma_f32_16x16x32_f16 v[146:149], v[134:137], v[162:165], v[146:149]
	v_exp_f32_e32 v231, v222
	v_rcp_f32_e32 v227, v227
	v_exp_f32_e32 v232, v223
	buffer_load_dwordx4 v[130:133], v189, s[16:19], s46 offen
	buffer_load_dwordx4 v[134:137], v208, s[16:19], s46 offen
	v_min_f32_e32 v233, s42, v224
	v_fma_f32 v230, v236, v230, v230
	v_exp_f32_e32 v234, v225
	s_waitcnt lgkmcnt(0)
	v_mfma_f32_16x16x32_f16 v[210:213], v[70:73], v[150:153], v[98:101]
	v_exp_f32_e32 v233, v233
	v_rcp_f32_e32 v230, v230
	v_add_f32_e32 v232, 1.0, v232
	v_mfma_f32_16x16x32_f16 v[214:217], v[74:77], v[150:153], v[102:105]
	v_fma_f32 v235, v233, s41, s41
	v_fma_f32 v236, -v228, v230, v230
	v_rcp_f32_e32 v232, v232
	v_fma_f32 v235, v231, v235, v235
	v_fma_f32 v198, v198, v227, v236
	v_rcp_f32_e32 v235, v235
	s_nop 0
	v_fma_f32 v231, -v233, v235, v235
	v_exp_f32_e32 v236, v198
	v_fma_f32 v199, v199, v232, v231
	v_exp_f32_e32 v231, v199
	v_add_f32_e32 v227, 1.0, v236
	v_add_f32_e32 v232, 1.0, v231
	v_fma_f32 v232, v234, v232, v232
	v_fma_f32 v227, v229, v227, v227
	v_rcp_f32_e32 v232, v232
	s_nop 0
	v_fma_f32 v231, -v231, v232, v232
	v_rcp_f32_e32 v227, v227
	s_nop 0
	v_fma_f32 v236, -v236, v227, v227
	v_cvt_pk_f16_f32 v247, v236, v231
	ds_write_b64 v206, v[246:247] offset:12288
	v_mfma_f32_16x16x32_f16 v[210:213], v[66:69], v[154:157], v[210:213]
	v_mfma_f32_16x16x32_f16 v[214:217], v[78:81], v[154:157], v[214:217]
	v_mov_b32_e32 v184, v246
	v_mov_b32_e32 v185, v247
	buffer_load_dwordx2 v[194:195], v209, s[20:23], s45 offen
	s_add_i32 s40, s40, 1
	s_add_i32 s44, s44, 0x1000
	s_waitcnt lgkmcnt(0)
	s_barrier
	ds_read_b128 v[158:161], v252 offset:4096
	ds_read_b128 v[162:165], v252 offset:5120
	ds_read_b128 v[166:169], v253 offset:6144
	ds_read_b128 v[170:173], v253 offset:7168
	v_mfma_f32_16x16x32_f16 v[218:221], v[82:85], v[150:153], v[106:109]
	v_mfma_f32_16x16x32_f16 v[222:225], v[90:93], v[150:153], v[110:113]
	v_mfma_f32_16x16x32_f16 v[218:221], v[86:89], v[154:157], v[218:221]
	v_mfma_f32_16x16x32_f16 v[222:225], v[94:97], v[154:157], v[222:225]
	s_waitcnt lgkmcnt(2)
	v_mfma_f32_16x16x32_f16 v[210:213], v[54:57], v[158:161], v[210:213]
	v_mfma_f32_16x16x32_f16 v[210:213], v[58:61], v[162:165], v[210:213]
	s_waitcnt lgkmcnt(0)
	v_mfma_f32_16x16x32_f16 v[210:213], v[62:65], v[166:169], v[210:213]
	v_mfma_f32_16x16x32_f16 v[210:213], v[50:53], v[170:173], v[210:213]
	s_waitcnt vmcnt(9)
	v_cvt_pk_f16_f32 v251, v192, v193
	ds_write_b32 v1, v251 offset:0
	ds_read_b128 v[150:153], v186 offset:6144
	ds_read_b128 v[154:157], v186 offset:7168
	s_add_i32 s45, s45, 0x100000
	s_add_i32 s46, s46, 0x4000
	s_movk_i32 s47, 0x0
	s_add_i32 s43, s40, -12
	s_lshl_b32 s43, s43, 12
	s_cmp_lt_u32 s40, 14
	s_cselect_b32 s43, s47, s43
	v_exp_f32_e32 v226, v210
	v_exp_f32_e32 v227, v211
	v_mfma_f32_16x16x32_f16 v[214:217], v[34:37], v[158:161], v[214:217]
	v_min_f32_e32 v228, s42, v212
	v_exp_f32_e32 v229, v213
	v_mfma_f32_16x16x32_f16 v[214:217], v[38:41], v[162:165], v[214:217]
	v_exp_f32_e32 v228, v228
	v_add_f32_e32 v227, 1.0, v227
	v_mfma_f32_16x16x32_f16 v[214:217], v[42:45], v[166:169], v[214:217]
	v_fma_f32 v230, v228, s41, s41
	v_rcp_f32_e32 v227, v227
	v_mfma_f32_16x16x32_f16 v[214:217], v[46:49], v[170:173], v[214:217]
	v_fma_f32 v230, v226, v230, v230
	v_rcp_f32_e32 v230, v230
	v_mfma_f32_16x16x32_f16 v[218:221], v[18:21], v[158:161], v[218:221]
	v_fma_f32 v226, -v228, v230, v230
	v_fma_f32 v200, v200, v227, v226
	v_mfma_f32_16x16x32_f16 v[218:221], v[14:17], v[162:165], v[218:221]
	v_exp_f32_e32 v226, v200
	s_nop 0
	v_add_f32_e32 v227, 1.0, v226
	v_mfma_f32_16x16x32_f16 v[218:221], v[10:13], v[166:169], v[218:221]
	v_fma_f32 v227, v229, v227, v227
	v_rcp_f32_e32 v227, v227
	v_mfma_f32_16x16x32_f16 v[218:221], v[26:29], v[170:173], v[218:221]
	v_fma_f32 v226, -v226, v227, v227
	v_exp_f32_e32 v231, v214
	v_mfma_f32_16x16x32_f16 v[222:225], v[2:5], v[158:161], v[222:225]
	v_exp_f32_e32 v232, v215
	v_min_f32_e32 v233, s42, v216
	v_mfma_f32_16x16x32_f16 v[222:225], v[6:9], v[162:165], v[222:225]
	v_exp_f32_e32 v234, v217
	v_exp_f32_e32 v233, v233
	v_mfma_f32_16x16x32_f16 v[222:225], v[22:25], v[166:169], v[222:225]
	v_exp_f32_e32 v236, v218
	v_add_f32_e32 v232, 1.0, v232
	v_mfma_f32_16x16x32_f16 v[222:225], v[30:33], v[170:173], v[222:225]
	v_fma_f32 v235, v233, s41, s41
	v_exp_f32_e32 v227, v219
	v_rcp_f32_e32 v232, v232
	v_fma_f32 v235, v231, v235, v235
	v_min_f32_e32 v228, s42, v220
	v_rcp_f32_e32 v235, v235
	s_nop 0
	v_fma_f32 v231, -v233, v235, v235
	v_exp_f32_e32 v229, v221
	v_fma_f32 v201, v201, v232, v231
	v_exp_f32_e32 v231, v201
	v_exp_f32_e32 v228, v228
	v_add_f32_e32 v232, 1.0, v231
	v_fma_f32 v232, v234, v232, v232
	v_add_f32_e32 v227, 1.0, v227
	v_rcp_f32_e32 v232, v232
	v_mfma_f32_16x16x32_f16 v[146:149], v[122:125], v[158:161], v[146:149]
	v_fma_f32 v231, -v231, v232, v232
	v_fma_f32 v230, v228, s41, s41
	v_cvt_pk_f16_f32 v246, v226, v231
	v_mfma_f32_16x16x32_f16 v[146:149], v[126:129], v[162:165], v[146:149]
	v_exp_f32_e32 v231, v222
	v_rcp_f32_e32 v227, v227
	v_exp_f32_e32 v232, v223
	buffer_load_dwordx4 v[122:125], v189, s[16:19], s46 offen
	buffer_load_dwordx4 v[126:129], v208, s[16:19], s46 offen
	v_min_f32_e32 v233, s42, v224
	v_fma_f32 v230, v236, v230, v230
	v_exp_f32_e32 v234, v225
	s_waitcnt lgkmcnt(0)
	v_mfma_f32_16x16x32_f16 v[210:213], v[70:73], v[150:153], v[98:101]
	v_exp_f32_e32 v233, v233
	v_rcp_f32_e32 v230, v230
	v_add_f32_e32 v232, 1.0, v232
	v_mfma_f32_16x16x32_f16 v[214:217], v[74:77], v[150:153], v[102:105]
	v_fma_f32 v235, v233, s41, s41
	v_fma_f32 v236, -v228, v230, v230
	v_rcp_f32_e32 v232, v232
	v_fma_f32 v235, v231, v235, v235
	v_fma_f32 v198, v198, v227, v236
	v_rcp_f32_e32 v235, v235
	s_nop 0
	v_fma_f32 v231, -v233, v235, v235
	v_exp_f32_e32 v236, v198
	v_fma_f32 v199, v199, v232, v231
	v_exp_f32_e32 v231, v199
	v_add_f32_e32 v227, 1.0, v236
	v_add_f32_e32 v232, 1.0, v231
	v_fma_f32 v232, v234, v232, v232
	v_fma_f32 v227, v229, v227, v227
	v_rcp_f32_e32 v232, v232
	s_nop 0
	v_fma_f32 v231, -v231, v232, v232
	v_rcp_f32_e32 v227, v227
	s_nop 0
	v_fma_f32 v236, -v236, v227, v227
	v_cvt_pk_f16_f32 v247, v236, v231
	ds_write_b64 v206, v[246:247] offset:8192
	v_mfma_f32_16x16x32_f16 v[210:213], v[66:69], v[154:157], v[210:213]
	v_mfma_f32_16x16x32_f16 v[214:217], v[78:81], v[154:157], v[214:217]
	v_mov_b32_e32 v237, v246
	v_mov_b32_e32 v238, v247
	buffer_load_dwordx2 v[192:193], v209, s[20:23], s45 offen
	s_add_i32 s40, s40, 1
	s_add_i32 s44, s44, 0x1000
	s_waitcnt lgkmcnt(0)
	s_barrier
	ds_read_b128 v[158:161], v252 offset:0
	ds_read_b128 v[162:165], v252 offset:1024
	ds_read_b128 v[166:169], v253 offset:2048
	ds_read_b128 v[170:173], v253 offset:3072
	v_mfma_f32_16x16x32_f16 v[218:221], v[82:85], v[150:153], v[106:109]
	v_mfma_f32_16x16x32_f16 v[222:225], v[90:93], v[150:153], v[110:113]
	v_mfma_f32_16x16x32_f16 v[218:221], v[86:89], v[154:157], v[218:221]
	v_mfma_f32_16x16x32_f16 v[222:225], v[94:97], v[154:157], v[222:225]
	s_waitcnt lgkmcnt(2)
	v_mfma_f32_16x16x32_f16 v[210:213], v[54:57], v[158:161], v[210:213]
	v_mfma_f32_16x16x32_f16 v[210:213], v[58:61], v[162:165], v[210:213]
	s_waitcnt lgkmcnt(0)
	v_mfma_f32_16x16x32_f16 v[210:213], v[62:65], v[166:169], v[210:213]
	v_mfma_f32_16x16x32_f16 v[210:213], v[50:53], v[170:173], v[210:213]
	s_waitcnt vmcnt(9)
	v_cvt_pk_f16_f32 v251, v190, v191
	ds_write_b32 v1, v251 offset:2048
	ds_read_b128 v[150:153], v186 offset:0
	ds_read_b128 v[154:157], v186 offset:1024
	s_add_i32 s45, s45, 0x100000
	s_add_i32 s46, s46, 0x4000
	s_movk_i32 s47, 0x1000
	s_add_i32 s43, s40, -12
	s_lshl_b32 s43, s43, 12
	s_cmp_lt_u32 s40, 14
	s_cselect_b32 s43, s47, s43
	v_exp_f32_e32 v226, v210
	v_exp_f32_e32 v227, v211
	v_mfma_f32_16x16x32_f16 v[214:217], v[34:37], v[158:161], v[214:217]
	v_min_f32_e32 v228, s42, v212
	v_exp_f32_e32 v229, v213
	v_mfma_f32_16x16x32_f16 v[214:217], v[38:41], v[162:165], v[214:217]
	v_exp_f32_e32 v228, v228
	v_add_f32_e32 v227, 1.0, v227
	v_mfma_f32_16x16x32_f16 v[214:217], v[42:45], v[166:169], v[214:217]
	v_fma_f32 v230, v228, s41, s41
	v_rcp_f32_e32 v227, v227
	v_mfma_f32_16x16x32_f16 v[214:217], v[46:49], v[170:173], v[214:217]
	v_fma_f32 v230, v226, v230, v230
	v_rcp_f32_e32 v230, v230
	v_mfma_f32_16x16x32_f16 v[218:221], v[18:21], v[158:161], v[218:221]
	v_fma_f32 v226, -v228, v230, v230
	v_fma_f32 v200, v200, v227, v226
	v_mfma_f32_16x16x32_f16 v[218:221], v[14:17], v[162:165], v[218:221]
	v_exp_f32_e32 v226, v200
	s_nop 0
	v_add_f32_e32 v227, 1.0, v226
	v_mfma_f32_16x16x32_f16 v[218:221], v[10:13], v[166:169], v[218:221]
	v_fma_f32 v227, v229, v227, v227
	v_rcp_f32_e32 v227, v227
	v_mfma_f32_16x16x32_f16 v[218:221], v[26:29], v[170:173], v[218:221]
	v_fma_f32 v226, -v226, v227, v227
	v_exp_f32_e32 v231, v214
	v_mfma_f32_16x16x32_f16 v[222:225], v[2:5], v[158:161], v[222:225]
	v_exp_f32_e32 v232, v215
	v_min_f32_e32 v233, s42, v216
	v_mfma_f32_16x16x32_f16 v[222:225], v[6:9], v[162:165], v[222:225]
	v_exp_f32_e32 v234, v217
	v_exp_f32_e32 v233, v233
	v_mfma_f32_16x16x32_f16 v[222:225], v[22:25], v[166:169], v[222:225]
	v_exp_f32_e32 v236, v218
	v_add_f32_e32 v232, 1.0, v232
	v_mfma_f32_16x16x32_f16 v[222:225], v[30:33], v[170:173], v[222:225]
	v_fma_f32 v235, v233, s41, s41
	v_exp_f32_e32 v227, v219
	v_rcp_f32_e32 v232, v232
	v_fma_f32 v235, v231, v235, v235
	v_min_f32_e32 v228, s42, v220
	v_rcp_f32_e32 v235, v235
	s_nop 0
	v_fma_f32 v231, -v233, v235, v235
	v_exp_f32_e32 v229, v221
	v_fma_f32 v201, v201, v232, v231
	v_exp_f32_e32 v231, v201
	v_exp_f32_e32 v228, v228
	v_add_f32_e32 v232, 1.0, v231
	v_fma_f32 v232, v234, v232, v232
	v_add_f32_e32 v227, 1.0, v227
	v_rcp_f32_e32 v232, v232
	v_mfma_f32_16x16x32_f16 v[146:149], v[114:117], v[158:161], v[146:149]
	v_fma_f32 v231, -v231, v232, v232
	v_fma_f32 v230, v228, s41, s41
	v_cvt_pk_f16_f32 v246, v226, v231
	v_mfma_f32_16x16x32_f16 v[146:149], v[118:121], v[162:165], v[146:149]
	v_exp_f32_e32 v231, v222
	v_rcp_f32_e32 v227, v227
	v_exp_f32_e32 v232, v223
	buffer_load_dwordx4 v[114:117], v189, s[16:19], s46 offen
	buffer_load_dwordx4 v[118:121], v208, s[16:19], s46 offen
	v_min_f32_e32 v233, s42, v224
	v_fma_f32 v230, v236, v230, v230
	v_exp_f32_e32 v234, v225
	s_waitcnt lgkmcnt(0)
	v_mfma_f32_16x16x32_f16 v[210:213], v[70:73], v[150:153], v[98:101]
	v_exp_f32_e32 v233, v233
	v_rcp_f32_e32 v230, v230
	v_add_f32_e32 v232, 1.0, v232
	v_mfma_f32_16x16x32_f16 v[214:217], v[74:77], v[150:153], v[102:105]
	v_fma_f32 v235, v233, s41, s41
	v_fma_f32 v236, -v228, v230, v230
	v_rcp_f32_e32 v232, v232
	v_fma_f32 v235, v231, v235, v235
	v_fma_f32 v198, v198, v227, v236
	v_rcp_f32_e32 v235, v235
	s_nop 0
	v_fma_f32 v231, -v233, v235, v235
	v_exp_f32_e32 v236, v198
	v_fma_f32 v199, v199, v232, v231
	v_exp_f32_e32 v231, v199
	v_add_f32_e32 v227, 1.0, v236
	v_add_f32_e32 v232, 1.0, v231
	v_fma_f32 v232, v234, v232, v232
	v_fma_f32 v227, v229, v227, v227
	v_rcp_f32_e32 v232, v232
	s_nop 0
	v_fma_f32 v231, -v231, v232, v232
	v_rcp_f32_e32 v227, v227
	s_nop 0
	v_fma_f32 v236, -v236, v227, v227
	v_cvt_pk_f16_f32 v247, v236, v231
	ds_write_b64 v206, v[246:247] offset:12288
	v_mfma_f32_16x16x32_f16 v[210:213], v[66:69], v[154:157], v[210:213]
	v_mfma_f32_16x16x32_f16 v[214:217], v[78:81], v[154:157], v[214:217]
	v_mov_b32_e32 v239, v246
	v_mov_b32_e32 v240, v247
	buffer_load_dwordx2 v[190:191], v209, s[20:23], s45 offen
	s_add_i32 s40, s40, 1
	s_add_i32 s44, s44, 0x1000
	s_waitcnt lgkmcnt(0)
	s_barrier
	ds_read_b128 v[158:161], v252 offset:4096
	ds_read_b128 v[162:165], v252 offset:5120
	ds_read_b128 v[166:169], v253 offset:6144
	ds_read_b128 v[170:173], v253 offset:7168
	v_mfma_f32_16x16x32_f16 v[218:221], v[82:85], v[150:153], v[106:109]
	v_mfma_f32_16x16x32_f16 v[222:225], v[90:93], v[150:153], v[110:113]
	v_mfma_f32_16x16x32_f16 v[218:221], v[86:89], v[154:157], v[218:221]
	v_mfma_f32_16x16x32_f16 v[222:225], v[94:97], v[154:157], v[222:225]
	s_waitcnt lgkmcnt(2)
	v_mfma_f32_16x16x32_f16 v[210:213], v[54:57], v[158:161], v[210:213]
	v_mfma_f32_16x16x32_f16 v[210:213], v[58:61], v[162:165], v[210:213]
	s_waitcnt lgkmcnt(0)
	v_mfma_f32_16x16x32_f16 v[210:213], v[62:65], v[166:169], v[210:213]
	v_mfma_f32_16x16x32_f16 v[210:213], v[50:53], v[170:173], v[210:213]
	s_waitcnt vmcnt(9)
	v_cvt_pk_f16_f32 v251, v196, v197
	ds_write_b32 v1, v251 offset:4096
	ds_read_b128 v[150:153], v186 offset:2048
	ds_read_b128 v[154:157], v186 offset:3072
	s_add_i32 s45, s45, 0x100000
	s_add_i32 s46, s46, 0x4000
	s_movk_i32 s47, 0x0
	s_add_i32 s43, s40, -12
	s_lshl_b32 s43, s43, 12
	s_cmp_lt_u32 s40, 14
	s_cselect_b32 s43, s47, s43
	v_exp_f32_e32 v226, v210
	v_exp_f32_e32 v227, v211
	v_mfma_f32_16x16x32_f16 v[214:217], v[34:37], v[158:161], v[214:217]
	v_min_f32_e32 v228, s42, v212
	v_exp_f32_e32 v229, v213
	v_mfma_f32_16x16x32_f16 v[214:217], v[38:41], v[162:165], v[214:217]
	v_exp_f32_e32 v228, v228
	v_add_f32_e32 v227, 1.0, v227
	v_mfma_f32_16x16x32_f16 v[214:217], v[42:45], v[166:169], v[214:217]
	v_fma_f32 v230, v228, s41, s41
	v_rcp_f32_e32 v227, v227
	v_mfma_f32_16x16x32_f16 v[214:217], v[46:49], v[170:173], v[214:217]
	v_fma_f32 v230, v226, v230, v230
	v_rcp_f32_e32 v230, v230
	v_mfma_f32_16x16x32_f16 v[218:221], v[18:21], v[158:161], v[218:221]
	v_fma_f32 v226, -v228, v230, v230
	v_fma_f32 v200, v200, v227, v226
	v_mfma_f32_16x16x32_f16 v[218:221], v[14:17], v[162:165], v[218:221]
	v_exp_f32_e32 v226, v200
	s_nop 0
	v_add_f32_e32 v227, 1.0, v226
	v_mfma_f32_16x16x32_f16 v[218:221], v[10:13], v[166:169], v[218:221]
	v_fma_f32 v227, v229, v227, v227
	v_rcp_f32_e32 v227, v227
	v_mfma_f32_16x16x32_f16 v[218:221], v[26:29], v[170:173], v[218:221]
	v_fma_f32 v226, -v226, v227, v227
	v_exp_f32_e32 v231, v214
	v_mfma_f32_16x16x32_f16 v[222:225], v[2:5], v[158:161], v[222:225]
	v_exp_f32_e32 v232, v215
	v_min_f32_e32 v233, s42, v216
	v_mfma_f32_16x16x32_f16 v[222:225], v[6:9], v[162:165], v[222:225]
	v_exp_f32_e32 v234, v217
	v_exp_f32_e32 v233, v233
	v_mfma_f32_16x16x32_f16 v[222:225], v[22:25], v[166:169], v[222:225]
	v_exp_f32_e32 v236, v218
	v_add_f32_e32 v232, 1.0, v232
	v_mfma_f32_16x16x32_f16 v[222:225], v[30:33], v[170:173], v[222:225]
	v_fma_f32 v235, v233, s41, s41
	v_exp_f32_e32 v227, v219
	v_rcp_f32_e32 v232, v232
	v_fma_f32 v235, v231, v235, v235
	v_min_f32_e32 v228, s42, v220
	v_rcp_f32_e32 v235, v235
	s_nop 0
	v_fma_f32 v231, -v233, v235, v235
	v_exp_f32_e32 v229, v221
	v_fma_f32 v201, v201, v232, v231
	v_exp_f32_e32 v231, v201
	v_exp_f32_e32 v228, v228
	v_add_f32_e32 v232, 1.0, v231
	v_fma_f32 v232, v234, v232, v232
	v_add_f32_e32 v227, 1.0, v227
	v_rcp_f32_e32 v232, v232
	v_mfma_f32_16x16x32_f16 v[146:149], v[138:141], v[158:161], v[146:149]
	v_fma_f32 v231, -v231, v232, v232
	v_fma_f32 v230, v228, s41, s41
	v_cvt_pk_f16_f32 v246, v226, v231
	v_mfma_f32_16x16x32_f16 v[146:149], v[142:145], v[162:165], v[146:149]
	v_exp_f32_e32 v231, v222
	v_rcp_f32_e32 v227, v227
	v_exp_f32_e32 v232, v223
	buffer_load_dwordx4 v[138:141], v189, s[16:19], s46 offen
	buffer_load_dwordx4 v[142:145], v208, s[16:19], s46 offen
	v_min_f32_e32 v233, s42, v224
	v_fma_f32 v230, v236, v230, v230
	v_exp_f32_e32 v234, v225
	s_waitcnt lgkmcnt(0)
	v_mfma_f32_16x16x32_f16 v[210:213], v[70:73], v[150:153], v[98:101]
	v_exp_f32_e32 v233, v233
	v_rcp_f32_e32 v230, v230
	v_add_f32_e32 v232, 1.0, v232
	v_mfma_f32_16x16x32_f16 v[214:217], v[74:77], v[150:153], v[102:105]
	v_fma_f32 v235, v233, s41, s41
	v_fma_f32 v236, -v228, v230, v230
	v_rcp_f32_e32 v232, v232
	v_fma_f32 v235, v231, v235, v235
	v_fma_f32 v198, v198, v227, v236
	v_rcp_f32_e32 v235, v235
	s_nop 0
	v_fma_f32 v231, -v233, v235, v235
	v_exp_f32_e32 v236, v198
	v_fma_f32 v199, v199, v232, v231
	v_exp_f32_e32 v231, v199
	v_add_f32_e32 v227, 1.0, v236
	v_add_f32_e32 v232, 1.0, v231
	v_fma_f32 v232, v234, v232, v232
	v_fma_f32 v227, v229, v227, v227
	v_rcp_f32_e32 v232, v232
	s_nop 0
	v_fma_f32 v231, -v231, v232, v232
	v_rcp_f32_e32 v227, v227
	s_nop 0
	v_fma_f32 v236, -v236, v227, v227
	v_cvt_pk_f16_f32 v247, v236, v231
	ds_write_b64 v206, v[246:247] offset:8192
	v_mfma_f32_16x16x32_f16 v[210:213], v[66:69], v[154:157], v[210:213]
	v_mfma_f32_16x16x32_f16 v[214:217], v[78:81], v[154:157], v[214:217]
	v_mov_b32_e32 v241, v246
	v_mov_b32_e32 v242, v247
	buffer_load_dwordx2 v[196:197], v209, s[20:23], s45 offen
	s_add_i32 s40, s40, 1
	s_add_i32 s44, s44, 0x1000
	s_waitcnt lgkmcnt(0)
	s_barrier
	ds_read_b128 v[158:161], v252 offset:0
	ds_read_b128 v[162:165], v252 offset:1024
	ds_read_b128 v[166:169], v253 offset:2048
	ds_read_b128 v[170:173], v253 offset:3072
	v_mfma_f32_16x16x32_f16 v[218:221], v[82:85], v[150:153], v[106:109]
	v_mfma_f32_16x16x32_f16 v[222:225], v[90:93], v[150:153], v[110:113]
	v_mfma_f32_16x16x32_f16 v[218:221], v[86:89], v[154:157], v[218:221]
	v_mfma_f32_16x16x32_f16 v[222:225], v[94:97], v[154:157], v[222:225]
	s_waitcnt lgkmcnt(2)
	v_mfma_f32_16x16x32_f16 v[210:213], v[54:57], v[158:161], v[210:213]
	v_mfma_f32_16x16x32_f16 v[210:213], v[58:61], v[162:165], v[210:213]
	s_waitcnt lgkmcnt(0)
	v_mfma_f32_16x16x32_f16 v[210:213], v[62:65], v[166:169], v[210:213]
	v_mfma_f32_16x16x32_f16 v[210:213], v[50:53], v[170:173], v[210:213]
	s_waitcnt vmcnt(9)
	v_cvt_pk_f16_f32 v251, v194, v195
	ds_write_b32 v1, v251 offset:6144
	ds_read_b128 v[150:153], v186 offset:4096
	ds_read_b128 v[154:157], v186 offset:5120
	s_add_i32 s45, s45, 0x100000
	s_add_i32 s46, s46, 0x4000
	s_movk_i32 s47, 0x1000
	s_add_i32 s43, s40, -12
	s_lshl_b32 s43, s43, 12
	s_cmp_lt_u32 s40, 14
	s_cselect_b32 s43, s47, s43
	v_exp_f32_e32 v226, v210
	v_exp_f32_e32 v227, v211
	v_mfma_f32_16x16x32_f16 v[214:217], v[34:37], v[158:161], v[214:217]
	v_min_f32_e32 v228, s42, v212
	v_exp_f32_e32 v229, v213
	v_mfma_f32_16x16x32_f16 v[214:217], v[38:41], v[162:165], v[214:217]
	v_exp_f32_e32 v228, v228
	v_add_f32_e32 v227, 1.0, v227
	v_mfma_f32_16x16x32_f16 v[214:217], v[42:45], v[166:169], v[214:217]
	v_fma_f32 v230, v228, s41, s41
	v_rcp_f32_e32 v227, v227
	v_mfma_f32_16x16x32_f16 v[214:217], v[46:49], v[170:173], v[214:217]
	v_fma_f32 v230, v226, v230, v230
	v_rcp_f32_e32 v230, v230
	v_mfma_f32_16x16x32_f16 v[218:221], v[18:21], v[158:161], v[218:221]
	v_fma_f32 v226, -v228, v230, v230
	v_fma_f32 v200, v200, v227, v226
	v_mfma_f32_16x16x32_f16 v[218:221], v[14:17], v[162:165], v[218:221]
	v_exp_f32_e32 v226, v200
	s_nop 0
	v_add_f32_e32 v227, 1.0, v226
	v_mfma_f32_16x16x32_f16 v[218:221], v[10:13], v[166:169], v[218:221]
	v_fma_f32 v227, v229, v227, v227
	v_rcp_f32_e32 v227, v227
	v_mfma_f32_16x16x32_f16 v[218:221], v[26:29], v[170:173], v[218:221]
	v_fma_f32 v226, -v226, v227, v227
	v_exp_f32_e32 v231, v214
	v_mfma_f32_16x16x32_f16 v[222:225], v[2:5], v[158:161], v[222:225]
	v_exp_f32_e32 v232, v215
	v_min_f32_e32 v233, s42, v216
	v_mfma_f32_16x16x32_f16 v[222:225], v[6:9], v[162:165], v[222:225]
	v_exp_f32_e32 v234, v217
	v_exp_f32_e32 v233, v233
	v_mfma_f32_16x16x32_f16 v[222:225], v[22:25], v[166:169], v[222:225]
	v_exp_f32_e32 v236, v218
	v_add_f32_e32 v232, 1.0, v232
	v_mfma_f32_16x16x32_f16 v[222:225], v[30:33], v[170:173], v[222:225]
	v_fma_f32 v235, v233, s41, s41
	v_exp_f32_e32 v227, v219
	v_rcp_f32_e32 v232, v232
	v_fma_f32 v235, v231, v235, v235
	v_min_f32_e32 v228, s42, v220
	v_rcp_f32_e32 v235, v235
	s_nop 0
	v_fma_f32 v231, -v233, v235, v235
	v_exp_f32_e32 v229, v221
	v_fma_f32 v201, v201, v232, v231
	v_exp_f32_e32 v231, v201
	v_exp_f32_e32 v228, v228
	v_add_f32_e32 v232, 1.0, v231
	v_fma_f32 v232, v234, v232, v232
	v_add_f32_e32 v227, 1.0, v227
	v_rcp_f32_e32 v232, v232
	v_mfma_f32_16x16x32_f16 v[146:149], v[130:133], v[158:161], v[146:149]
	v_fma_f32 v231, -v231, v232, v232
	v_fma_f32 v230, v228, s41, s41
	v_cvt_pk_f16_f32 v246, v226, v231
	v_mfma_f32_16x16x32_f16 v[146:149], v[134:137], v[162:165], v[146:149]
	v_exp_f32_e32 v231, v222
	v_rcp_f32_e32 v227, v227
	v_exp_f32_e32 v232, v223
	buffer_load_dwordx4 v[130:133], v189, s[16:19], s46 offen
	buffer_load_dwordx4 v[134:137], v208, s[16:19], s46 offen
	v_min_f32_e32 v233, s42, v224
	v_fma_f32 v230, v236, v230, v230
	v_exp_f32_e32 v234, v225
	s_waitcnt lgkmcnt(0)
	v_mfma_f32_16x16x32_f16 v[210:213], v[70:73], v[150:153], v[98:101]
	v_exp_f32_e32 v233, v233
	v_rcp_f32_e32 v230, v230
	v_add_f32_e32 v232, 1.0, v232
	v_mfma_f32_16x16x32_f16 v[214:217], v[74:77], v[150:153], v[102:105]
	v_fma_f32 v235, v233, s41, s41
	v_fma_f32 v236, -v228, v230, v230
	v_rcp_f32_e32 v232, v232
	v_fma_f32 v235, v231, v235, v235
	v_fma_f32 v198, v198, v227, v236
	v_rcp_f32_e32 v235, v235
	s_nop 0
	v_fma_f32 v231, -v233, v235, v235
	v_exp_f32_e32 v236, v198
	v_fma_f32 v199, v199, v232, v231
	v_exp_f32_e32 v231, v199
	v_add_f32_e32 v227, 1.0, v236
	v_add_f32_e32 v232, 1.0, v231
	v_fma_f32 v232, v234, v232, v232
	v_fma_f32 v227, v229, v227, v227
	v_rcp_f32_e32 v232, v232
	s_nop 0
	v_fma_f32 v231, -v231, v232, v232
	v_rcp_f32_e32 v227, v227
	s_nop 0
	v_fma_f32 v236, -v236, v227, v227
	v_cvt_pk_f16_f32 v247, v236, v231
	ds_write_b64 v206, v[246:247] offset:12288
	v_mfma_f32_16x16x32_f16 v[210:213], v[66:69], v[154:157], v[210:213]
	v_mfma_f32_16x16x32_f16 v[214:217], v[78:81], v[154:157], v[214:217]
	v_mov_b32_e32 v243, v246
	v_mov_b32_e32 v244, v247
	buffer_load_dwordx2 v[194:195], v209, s[20:23], s45 offen
	s_add_i32 s40, s40, 1
	s_add_i32 s44, s44, 0x1000
	s_waitcnt lgkmcnt(0)
	s_barrier
	ds_read_b128 v[158:161], v252 offset:4096
	ds_read_b128 v[162:165], v252 offset:5120
	ds_read_b128 v[166:169], v253 offset:6144
	ds_read_b128 v[170:173], v253 offset:7168
	v_mfma_f32_16x16x32_f16 v[218:221], v[82:85], v[150:153], v[106:109]
	v_mfma_f32_16x16x32_f16 v[222:225], v[90:93], v[150:153], v[110:113]
	v_mfma_f32_16x16x32_f16 v[218:221], v[86:89], v[154:157], v[218:221]
	v_mfma_f32_16x16x32_f16 v[222:225], v[94:97], v[154:157], v[222:225]
	s_waitcnt lgkmcnt(2)
	v_mfma_f32_16x16x32_f16 v[210:213], v[54:57], v[158:161], v[210:213]
	v_mfma_f32_16x16x32_f16 v[210:213], v[58:61], v[162:165], v[210:213]
	s_waitcnt lgkmcnt(0)
	v_mfma_f32_16x16x32_f16 v[210:213], v[62:65], v[166:169], v[210:213]
	v_mfma_f32_16x16x32_f16 v[210:213], v[50:53], v[170:173], v[210:213]
	s_waitcnt vmcnt(9)
	v_cvt_pk_f16_f32 v251, v192, v193
	ds_write_b32 v1, v251 offset:0
	ds_read_b128 v[150:153], v186 offset:6144
	ds_read_b128 v[154:157], v186 offset:7168
	s_add_i32 s45, s45, 0x100000
	s_add_i32 s46, s46, 0x4000
	s_movk_i32 s47, 0x0
	s_add_i32 s43, s40, -12
	s_lshl_b32 s43, s43, 12
	s_cmp_lt_u32 s40, 14
	s_cselect_b32 s43, s47, s43
	v_exp_f32_e32 v226, v210
	v_exp_f32_e32 v227, v211
	v_mfma_f32_16x16x32_f16 v[214:217], v[34:37], v[158:161], v[214:217]
	v_min_f32_e32 v228, s42, v212
	v_exp_f32_e32 v229, v213
	v_mfma_f32_16x16x32_f16 v[214:217], v[38:41], v[162:165], v[214:217]
	v_exp_f32_e32 v228, v228
	v_add_f32_e32 v227, 1.0, v227
	v_mfma_f32_16x16x32_f16 v[214:217], v[42:45], v[166:169], v[214:217]
	v_fma_f32 v230, v228, s41, s41
	v_rcp_f32_e32 v227, v227
	v_mfma_f32_16x16x32_f16 v[214:217], v[46:49], v[170:173], v[214:217]
	v_fma_f32 v230, v226, v230, v230
	v_rcp_f32_e32 v230, v230
	v_mfma_f32_16x16x32_f16 v[218:221], v[18:21], v[158:161], v[218:221]
	v_fma_f32 v226, -v228, v230, v230
	v_fma_f32 v200, v200, v227, v226
	v_mfma_f32_16x16x32_f16 v[218:221], v[14:17], v[162:165], v[218:221]
	v_exp_f32_e32 v226, v200
	s_nop 0
	v_add_f32_e32 v227, 1.0, v226
	v_mfma_f32_16x16x32_f16 v[218:221], v[10:13], v[166:169], v[218:221]
	v_fma_f32 v227, v229, v227, v227
	v_rcp_f32_e32 v227, v227
	v_mfma_f32_16x16x32_f16 v[218:221], v[26:29], v[170:173], v[218:221]
	v_fma_f32 v226, -v226, v227, v227
	v_exp_f32_e32 v231, v214
	v_mfma_f32_16x16x32_f16 v[222:225], v[2:5], v[158:161], v[222:225]
	v_exp_f32_e32 v232, v215
	v_min_f32_e32 v233, s42, v216
	v_mfma_f32_16x16x32_f16 v[222:225], v[6:9], v[162:165], v[222:225]
	v_exp_f32_e32 v234, v217
	v_exp_f32_e32 v233, v233
	v_mfma_f32_16x16x32_f16 v[222:225], v[22:25], v[166:169], v[222:225]
	v_exp_f32_e32 v236, v218
	v_add_f32_e32 v232, 1.0, v232
	v_mfma_f32_16x16x32_f16 v[222:225], v[30:33], v[170:173], v[222:225]
	v_fma_f32 v235, v233, s41, s41
	v_exp_f32_e32 v227, v219
	v_rcp_f32_e32 v232, v232
	v_fma_f32 v235, v231, v235, v235
	v_min_f32_e32 v228, s42, v220
	v_rcp_f32_e32 v235, v235
	s_nop 0
	v_fma_f32 v231, -v233, v235, v235
	v_exp_f32_e32 v229, v221
	v_fma_f32 v201, v201, v232, v231
	v_exp_f32_e32 v231, v201
	v_exp_f32_e32 v228, v228
	v_add_f32_e32 v232, 1.0, v231
	v_fma_f32 v232, v234, v232, v232
	v_add_f32_e32 v227, 1.0, v227
	v_rcp_f32_e32 v232, v232
	v_mfma_f32_16x16x32_f16 v[146:149], v[122:125], v[158:161], v[146:149]
	v_fma_f32 v231, -v231, v232, v232
	v_fma_f32 v230, v228, s41, s41
	v_cvt_pk_f16_f32 v246, v226, v231
	v_mfma_f32_16x16x32_f16 v[146:149], v[126:129], v[162:165], v[146:149]
	v_exp_f32_e32 v231, v222
	v_rcp_f32_e32 v227, v227
	v_exp_f32_e32 v232, v223
	buffer_load_dwordx4 v[122:125], v189, s[16:19], s46 offen
	buffer_load_dwordx4 v[126:129], v208, s[16:19], s46 offen
	v_min_f32_e32 v233, s42, v224
	v_fma_f32 v230, v236, v230, v230
	v_exp_f32_e32 v234, v225
	s_waitcnt lgkmcnt(0)
	v_mfma_f32_16x16x32_f16 v[210:213], v[70:73], v[150:153], v[98:101]
	v_exp_f32_e32 v233, v233
	v_rcp_f32_e32 v230, v230
	v_add_f32_e32 v232, 1.0, v232
	v_mfma_f32_16x16x32_f16 v[214:217], v[74:77], v[150:153], v[102:105]
	v_fma_f32 v235, v233, s41, s41
	v_fma_f32 v236, -v228, v230, v230
	v_rcp_f32_e32 v232, v232
	v_fma_f32 v235, v231, v235, v235
	v_fma_f32 v198, v198, v227, v236
	v_rcp_f32_e32 v235, v235
	s_nop 0
	v_fma_f32 v231, -v233, v235, v235
	v_exp_f32_e32 v236, v198
	v_fma_f32 v199, v199, v232, v231
	v_exp_f32_e32 v231, v199
	v_add_f32_e32 v227, 1.0, v236
	v_add_f32_e32 v232, 1.0, v231
	v_fma_f32 v232, v234, v232, v232
	v_fma_f32 v227, v229, v227, v227
	v_rcp_f32_e32 v232, v232
	s_nop 0
	v_fma_f32 v231, -v231, v232, v232
	v_rcp_f32_e32 v227, v227
	s_nop 0
	v_fma_f32 v236, -v236, v227, v227
	v_cvt_pk_f16_f32 v247, v236, v231
	ds_write_b64 v206, v[246:247] offset:8192
	v_mfma_f32_16x16x32_f16 v[210:213], v[66:69], v[154:157], v[210:213]
	v_mfma_f32_16x16x32_f16 v[214:217], v[78:81], v[154:157], v[214:217]
	v_mov_b32_e32 v245, v246
	v_mov_b32_e32 v187, v247
	buffer_load_dwordx2 v[192:193], v209, s[20:23], s45 offen
	s_add_i32 s40, s40, 1
	s_add_i32 s44, s44, 0x1000
	s_waitcnt lgkmcnt(0)
	s_barrier
	ds_read_b128 v[158:161], v252 offset:0
	ds_read_b128 v[162:165], v252 offset:1024
	ds_read_b128 v[166:169], v253 offset:2048
	ds_read_b128 v[170:173], v253 offset:3072
	v_mfma_f32_16x16x32_f16 v[218:221], v[82:85], v[150:153], v[106:109]
	v_mfma_f32_16x16x32_f16 v[222:225], v[90:93], v[150:153], v[110:113]
	v_mfma_f32_16x16x32_f16 v[218:221], v[86:89], v[154:157], v[218:221]
	v_mfma_f32_16x16x32_f16 v[222:225], v[94:97], v[154:157], v[222:225]
	s_waitcnt lgkmcnt(2)
	v_mfma_f32_16x16x32_f16 v[210:213], v[54:57], v[158:161], v[210:213]
	v_mfma_f32_16x16x32_f16 v[210:213], v[58:61], v[162:165], v[210:213]
	s_waitcnt lgkmcnt(0)
	v_mfma_f32_16x16x32_f16 v[210:213], v[62:65], v[166:169], v[210:213]
	v_mfma_f32_16x16x32_f16 v[210:213], v[50:53], v[170:173], v[210:213]
	s_waitcnt vmcnt(9)
	v_cvt_pk_f16_f32 v251, v190, v191
	ds_write_b32 v1, v251 offset:2048
	ds_read_b128 v[150:153], v186 offset:0
	ds_read_b128 v[154:157], v186 offset:1024
	s_add_i32 s45, s45, 0x100000
	s_add_i32 s46, s46, 0x4000
	s_movk_i32 s47, 0x1000
	s_add_i32 s43, s40, -12
	s_lshl_b32 s43, s43, 12
	s_cmp_lt_u32 s40, 14
	s_cselect_b32 s43, s47, s43
	v_exp_f32_e32 v226, v210
	v_exp_f32_e32 v227, v211
	v_mfma_f32_16x16x32_f16 v[214:217], v[34:37], v[158:161], v[214:217]
	v_min_f32_e32 v228, s42, v212
	v_exp_f32_e32 v229, v213
	v_mfma_f32_16x16x32_f16 v[214:217], v[38:41], v[162:165], v[214:217]
	v_exp_f32_e32 v228, v228
	v_add_f32_e32 v227, 1.0, v227
	v_mfma_f32_16x16x32_f16 v[214:217], v[42:45], v[166:169], v[214:217]
	v_fma_f32 v230, v228, s41, s41
	v_rcp_f32_e32 v227, v227
	v_mfma_f32_16x16x32_f16 v[214:217], v[46:49], v[170:173], v[214:217]
	v_fma_f32 v230, v226, v230, v230
	v_rcp_f32_e32 v230, v230
	v_mfma_f32_16x16x32_f16 v[218:221], v[18:21], v[158:161], v[218:221]
	v_fma_f32 v226, -v228, v230, v230
	v_fma_f32 v200, v200, v227, v226
	v_mfma_f32_16x16x32_f16 v[218:221], v[14:17], v[162:165], v[218:221]
	v_exp_f32_e32 v226, v200
	s_nop 0
	v_add_f32_e32 v227, 1.0, v226
	v_mfma_f32_16x16x32_f16 v[218:221], v[10:13], v[166:169], v[218:221]
	v_fma_f32 v227, v229, v227, v227
	v_rcp_f32_e32 v227, v227
	v_mfma_f32_16x16x32_f16 v[218:221], v[26:29], v[170:173], v[218:221]
	v_fma_f32 v226, -v226, v227, v227
	v_exp_f32_e32 v231, v214
	v_mfma_f32_16x16x32_f16 v[222:225], v[2:5], v[158:161], v[222:225]
	v_exp_f32_e32 v232, v215
	v_min_f32_e32 v233, s42, v216
	v_mfma_f32_16x16x32_f16 v[222:225], v[6:9], v[162:165], v[222:225]
	v_exp_f32_e32 v234, v217
	v_exp_f32_e32 v233, v233
	v_mfma_f32_16x16x32_f16 v[222:225], v[22:25], v[166:169], v[222:225]
	v_exp_f32_e32 v236, v218
	v_add_f32_e32 v232, 1.0, v232
	v_mfma_f32_16x16x32_f16 v[222:225], v[30:33], v[170:173], v[222:225]
	v_fma_f32 v235, v233, s41, s41
	v_exp_f32_e32 v227, v219
	v_rcp_f32_e32 v232, v232
	v_fma_f32 v235, v231, v235, v235
	v_min_f32_e32 v228, s42, v220
	v_rcp_f32_e32 v235, v235
	s_nop 0
	v_fma_f32 v231, -v233, v235, v235
	v_exp_f32_e32 v229, v221
	v_fma_f32 v201, v201, v232, v231
	v_exp_f32_e32 v231, v201
	v_exp_f32_e32 v228, v228
	v_add_f32_e32 v232, 1.0, v231
	v_fma_f32 v232, v234, v232, v232
	v_add_f32_e32 v227, 1.0, v227
	v_rcp_f32_e32 v232, v232
	v_mfma_f32_16x16x32_f16 v[146:149], v[114:117], v[158:161], v[146:149]
	v_fma_f32 v231, -v231, v232, v232
	v_fma_f32 v230, v228, s41, s41
	v_cvt_pk_f16_f32 v246, v226, v231
	v_mfma_f32_16x16x32_f16 v[146:149], v[118:121], v[162:165], v[146:149]
	v_exp_f32_e32 v231, v222
	v_rcp_f32_e32 v227, v227
	v_exp_f32_e32 v232, v223
	buffer_load_dwordx4 v[114:117], v189, s[16:19], s46 offen
	buffer_load_dwordx4 v[118:121], v208, s[16:19], s46 offen
	v_min_f32_e32 v233, s42, v224
	v_fma_f32 v230, v236, v230, v230
	v_exp_f32_e32 v234, v225
	s_waitcnt lgkmcnt(0)
	v_mfma_f32_16x16x32_f16 v[210:213], v[70:73], v[150:153], v[98:101]
	v_exp_f32_e32 v233, v233
	v_rcp_f32_e32 v230, v230
	v_add_f32_e32 v232, 1.0, v232
	v_mfma_f32_16x16x32_f16 v[214:217], v[74:77], v[150:153], v[102:105]
	v_fma_f32 v235, v233, s41, s41
	v_fma_f32 v236, -v228, v230, v230
	v_rcp_f32_e32 v232, v232
	v_fma_f32 v235, v231, v235, v235
	v_fma_f32 v198, v198, v227, v236
	v_rcp_f32_e32 v235, v235
	s_nop 0
	v_fma_f32 v231, -v233, v235, v235
	v_exp_f32_e32 v236, v198
	v_fma_f32 v199, v199, v232, v231
	v_exp_f32_e32 v231, v199
	v_add_f32_e32 v227, 1.0, v236
	v_add_f32_e32 v232, 1.0, v231
	v_fma_f32 v232, v234, v232, v232
	v_fma_f32 v227, v229, v227, v227
	v_rcp_f32_e32 v232, v232
	s_nop 0
	v_fma_f32 v231, -v231, v232, v232
	v_rcp_f32_e32 v227, v227
	s_nop 0
	v_fma_f32 v236, -v236, v227, v227
	v_cvt_pk_f16_f32 v247, v236, v231
	ds_write_b64 v206, v[246:247] offset:12288
	v_mfma_f32_16x16x32_f16 v[210:213], v[66:69], v[154:157], v[210:213]
	v_mfma_f32_16x16x32_f16 v[214:217], v[78:81], v[154:157], v[214:217]
	v_mov_b32_e32 v188, v246
	v_mov_b32_e32 v202, v247
	buffer_load_dwordx2 v[190:191], v209, s[20:23], s45 offen
	s_add_i32 s40, s40, 1
	s_add_i32 s44, s44, 0x1000
	s_waitcnt lgkmcnt(0)
	s_barrier
	ds_read_b128 v[158:161], v252 offset:4096
	ds_read_b128 v[162:165], v252 offset:5120
	ds_read_b128 v[166:169], v253 offset:6144
	ds_read_b128 v[170:173], v253 offset:7168
	v_mfma_f32_16x16x32_f16 v[218:221], v[82:85], v[150:153], v[106:109]
	v_mfma_f32_16x16x32_f16 v[222:225], v[90:93], v[150:153], v[110:113]
	v_mfma_f32_16x16x32_f16 v[218:221], v[86:89], v[154:157], v[218:221]
	v_mfma_f32_16x16x32_f16 v[222:225], v[94:97], v[154:157], v[222:225]
	s_waitcnt lgkmcnt(2)
	v_mfma_f32_16x16x32_f16 v[210:213], v[54:57], v[158:161], v[210:213]
	v_mfma_f32_16x16x32_f16 v[210:213], v[58:61], v[162:165], v[210:213]
	s_waitcnt lgkmcnt(0)
	v_mfma_f32_16x16x32_f16 v[210:213], v[62:65], v[166:169], v[210:213]
	v_mfma_f32_16x16x32_f16 v[210:213], v[50:53], v[170:173], v[210:213]
	s_waitcnt vmcnt(9)
	v_cvt_pk_f16_f32 v251, v196, v197
	ds_write_b32 v1, v251 offset:4096
	ds_read_b128 v[150:153], v186 offset:2048
	ds_read_b128 v[154:157], v186 offset:3072
	s_add_i32 s45, s45, 0x100000
	s_add_i32 s46, s46, 0x4000
	s_movk_i32 s47, 0x0
	s_add_i32 s43, s40, -12
	s_lshl_b32 s43, s43, 12
	s_cmp_lt_u32 s40, 14
	s_cselect_b32 s43, s47, s43
	v_exp_f32_e32 v226, v210
	v_exp_f32_e32 v227, v211
	v_mfma_f32_16x16x32_f16 v[214:217], v[34:37], v[158:161], v[214:217]
	v_min_f32_e32 v228, s42, v212
	v_exp_f32_e32 v229, v213
	v_mfma_f32_16x16x32_f16 v[214:217], v[38:41], v[162:165], v[214:217]
	v_exp_f32_e32 v228, v228
	v_add_f32_e32 v227, 1.0, v227
	v_mfma_f32_16x16x32_f16 v[214:217], v[42:45], v[166:169], v[214:217]
	v_fma_f32 v230, v228, s41, s41
	v_rcp_f32_e32 v227, v227
	v_mfma_f32_16x16x32_f16 v[214:217], v[46:49], v[170:173], v[214:217]
	v_fma_f32 v230, v226, v230, v230
	v_rcp_f32_e32 v230, v230
	v_mfma_f32_16x16x32_f16 v[218:221], v[18:21], v[158:161], v[218:221]
	v_fma_f32 v226, -v228, v230, v230
	v_fma_f32 v200, v200, v227, v226
	v_mfma_f32_16x16x32_f16 v[218:221], v[14:17], v[162:165], v[218:221]
	v_exp_f32_e32 v226, v200
	s_nop 0
	v_add_f32_e32 v227, 1.0, v226
	v_mfma_f32_16x16x32_f16 v[218:221], v[10:13], v[166:169], v[218:221]
	v_fma_f32 v227, v229, v227, v227
	v_rcp_f32_e32 v227, v227
	v_mfma_f32_16x16x32_f16 v[218:221], v[26:29], v[170:173], v[218:221]
	v_fma_f32 v226, -v226, v227, v227
	v_exp_f32_e32 v231, v214
	v_mfma_f32_16x16x32_f16 v[222:225], v[2:5], v[158:161], v[222:225]
	v_exp_f32_e32 v232, v215
	v_min_f32_e32 v233, s42, v216
	v_mfma_f32_16x16x32_f16 v[222:225], v[6:9], v[162:165], v[222:225]
	v_exp_f32_e32 v234, v217
	v_exp_f32_e32 v233, v233
	v_mfma_f32_16x16x32_f16 v[222:225], v[22:25], v[166:169], v[222:225]
	v_exp_f32_e32 v236, v218
	v_add_f32_e32 v232, 1.0, v232
	v_mfma_f32_16x16x32_f16 v[222:225], v[30:33], v[170:173], v[222:225]
	v_fma_f32 v235, v233, s41, s41
	v_exp_f32_e32 v227, v219
	v_rcp_f32_e32 v232, v232
	v_fma_f32 v235, v231, v235, v235
	v_min_f32_e32 v228, s42, v220
	v_rcp_f32_e32 v235, v235
	s_nop 0
	v_fma_f32 v231, -v233, v235, v235
	v_exp_f32_e32 v229, v221
	v_fma_f32 v201, v201, v232, v231
	v_exp_f32_e32 v231, v201
	v_exp_f32_e32 v228, v228
	v_add_f32_e32 v232, 1.0, v231
	v_fma_f32 v232, v234, v232, v232
	v_add_f32_e32 v227, 1.0, v227
	v_rcp_f32_e32 v232, v232
	v_mfma_f32_16x16x32_f16 v[146:149], v[138:141], v[158:161], v[146:149]
	v_fma_f32 v231, -v231, v232, v232
	v_fma_f32 v230, v228, s41, s41
	v_cvt_pk_f16_f32 v246, v226, v231
	v_mfma_f32_16x16x32_f16 v[146:149], v[142:145], v[162:165], v[146:149]
	v_exp_f32_e32 v231, v222
	v_rcp_f32_e32 v227, v227
	v_exp_f32_e32 v232, v223
	buffer_load_dwordx4 v[138:141], v189, s[16:19], s46 offen
	buffer_load_dwordx4 v[142:145], v208, s[16:19], s46 offen
	v_min_f32_e32 v233, s42, v224
	v_fma_f32 v230, v236, v230, v230
	v_exp_f32_e32 v234, v225
	s_waitcnt lgkmcnt(0)
	v_mfma_f32_16x16x32_f16 v[210:213], v[70:73], v[150:153], v[98:101]
	v_exp_f32_e32 v233, v233
	v_rcp_f32_e32 v230, v230
	v_add_f32_e32 v232, 1.0, v232
	v_mfma_f32_16x16x32_f16 v[214:217], v[74:77], v[150:153], v[102:105]
	v_fma_f32 v235, v233, s41, s41
	v_fma_f32 v236, -v228, v230, v230
	v_rcp_f32_e32 v232, v232
	v_fma_f32 v235, v231, v235, v235
	v_fma_f32 v198, v198, v227, v236
	v_rcp_f32_e32 v235, v235
	s_nop 0
	v_fma_f32 v231, -v233, v235, v235
	v_exp_f32_e32 v236, v198
	v_fma_f32 v199, v199, v232, v231
	v_exp_f32_e32 v231, v199
	v_add_f32_e32 v227, 1.0, v236
	v_add_f32_e32 v232, 1.0, v231
	v_fma_f32 v232, v234, v232, v232
	v_fma_f32 v227, v229, v227, v227
	v_rcp_f32_e32 v232, v232
	s_nop 0
	v_fma_f32 v231, -v231, v232, v232
	v_rcp_f32_e32 v227, v227
	s_nop 0
	v_fma_f32 v236, -v236, v227, v227
	v_cvt_pk_f16_f32 v247, v236, v231
	ds_write_b64 v206, v[246:247] offset:8192
	v_mfma_f32_16x16x32_f16 v[210:213], v[66:69], v[154:157], v[210:213]
	v_mfma_f32_16x16x32_f16 v[214:217], v[78:81], v[154:157], v[214:217]
	v_mov_b32_e32 v203, v246
	v_mov_b32_e32 v204, v247
	buffer_load_dwordx2 v[196:197], v209, s[20:23], s45 offen
	s_add_i32 s40, s40, 1
	s_add_i32 s44, s44, 0x1000
	s_waitcnt lgkmcnt(0)
	s_barrier
	ds_read_b128 v[158:161], v252 offset:0
	ds_read_b128 v[162:165], v252 offset:1024
	ds_read_b128 v[166:169], v253 offset:2048
	ds_read_b128 v[170:173], v253 offset:3072
	v_mfma_f32_16x16x32_f16 v[218:221], v[82:85], v[150:153], v[106:109]
	v_mfma_f32_16x16x32_f16 v[222:225], v[90:93], v[150:153], v[110:113]
	v_mfma_f32_16x16x32_f16 v[218:221], v[86:89], v[154:157], v[218:221]
	v_mfma_f32_16x16x32_f16 v[222:225], v[94:97], v[154:157], v[222:225]
	s_waitcnt lgkmcnt(2)
	v_mfma_f32_16x16x32_f16 v[210:213], v[54:57], v[158:161], v[210:213]
	v_mfma_f32_16x16x32_f16 v[210:213], v[58:61], v[162:165], v[210:213]
	s_waitcnt lgkmcnt(0)
	v_mfma_f32_16x16x32_f16 v[210:213], v[62:65], v[166:169], v[210:213]
	v_mfma_f32_16x16x32_f16 v[210:213], v[50:53], v[170:173], v[210:213]
	s_waitcnt vmcnt(9)
	v_cvt_pk_f16_f32 v251, v194, v195
	ds_write_b32 v1, v251 offset:6144
	ds_read_b128 v[150:153], v186 offset:4096
	ds_read_b128 v[154:157], v186 offset:5120
	s_add_i32 s45, s45, 0x100000
	s_add_i32 s46, s46, 0x4000
	s_movk_i32 s47, 0x1000
	s_add_i32 s43, s40, -12
	s_lshl_b32 s43, s43, 12
	s_cmp_lt_u32 s40, 14
	s_cselect_b32 s43, s47, s43
	v_exp_f32_e32 v226, v210
	v_exp_f32_e32 v227, v211
	v_mfma_f32_16x16x32_f16 v[214:217], v[34:37], v[158:161], v[214:217]
	v_min_f32_e32 v228, s42, v212
	v_exp_f32_e32 v229, v213
	v_mfma_f32_16x16x32_f16 v[214:217], v[38:41], v[162:165], v[214:217]
	v_exp_f32_e32 v228, v228
	v_add_f32_e32 v227, 1.0, v227
	v_mfma_f32_16x16x32_f16 v[214:217], v[42:45], v[166:169], v[214:217]
	v_fma_f32 v230, v228, s41, s41
	v_rcp_f32_e32 v227, v227
	v_mfma_f32_16x16x32_f16 v[214:217], v[46:49], v[170:173], v[214:217]
	v_fma_f32 v230, v226, v230, v230
	v_rcp_f32_e32 v230, v230
	v_mfma_f32_16x16x32_f16 v[218:221], v[18:21], v[158:161], v[218:221]
	v_fma_f32 v226, -v228, v230, v230
	v_fma_f32 v200, v200, v227, v226
	v_mfma_f32_16x16x32_f16 v[218:221], v[14:17], v[162:165], v[218:221]
	v_exp_f32_e32 v226, v200
	s_nop 0
	v_add_f32_e32 v227, 1.0, v226
	v_mfma_f32_16x16x32_f16 v[218:221], v[10:13], v[166:169], v[218:221]
	v_fma_f32 v227, v229, v227, v227
	v_rcp_f32_e32 v227, v227
	v_mfma_f32_16x16x32_f16 v[218:221], v[26:29], v[170:173], v[218:221]
	v_fma_f32 v226, -v226, v227, v227
	v_exp_f32_e32 v231, v214
	v_mfma_f32_16x16x32_f16 v[222:225], v[2:5], v[158:161], v[222:225]
	v_exp_f32_e32 v232, v215
	v_min_f32_e32 v233, s42, v216
	v_mfma_f32_16x16x32_f16 v[222:225], v[6:9], v[162:165], v[222:225]
	v_exp_f32_e32 v234, v217
	v_exp_f32_e32 v233, v233
	v_mfma_f32_16x16x32_f16 v[222:225], v[22:25], v[166:169], v[222:225]
	v_exp_f32_e32 v236, v218
	v_add_f32_e32 v232, 1.0, v232
	v_mfma_f32_16x16x32_f16 v[222:225], v[30:33], v[170:173], v[222:225]
	v_fma_f32 v235, v233, s41, s41
	v_exp_f32_e32 v227, v219
	v_rcp_f32_e32 v232, v232
	v_fma_f32 v235, v231, v235, v235
	v_min_f32_e32 v228, s42, v220
	v_rcp_f32_e32 v235, v235
	s_nop 0
	v_fma_f32 v231, -v233, v235, v235
	v_exp_f32_e32 v229, v221
	v_fma_f32 v201, v201, v232, v231
	v_exp_f32_e32 v231, v201
	v_exp_f32_e32 v228, v228
	v_add_f32_e32 v232, 1.0, v231
	v_fma_f32 v232, v234, v232, v232
	v_add_f32_e32 v227, 1.0, v227
	v_rcp_f32_e32 v232, v232
	v_mfma_f32_16x16x32_f16 v[146:149], v[130:133], v[158:161], v[146:149]
	v_fma_f32 v231, -v231, v232, v232
	v_fma_f32 v230, v228, s41, s41
	v_cvt_pk_f16_f32 v246, v226, v231
	v_mfma_f32_16x16x32_f16 v[146:149], v[134:137], v[162:165], v[146:149]
	v_exp_f32_e32 v231, v222
	v_rcp_f32_e32 v227, v227
	v_exp_f32_e32 v232, v223
	buffer_load_dwordx4 v[130:133], v189, s[16:19], s46 offen
	buffer_load_dwordx4 v[134:137], v208, s[16:19], s46 offen
	v_min_f32_e32 v233, s42, v224
	v_fma_f32 v230, v236, v230, v230
	v_exp_f32_e32 v234, v225
	s_waitcnt lgkmcnt(0)
	v_mfma_f32_16x16x32_f16 v[210:213], v[70:73], v[150:153], v[98:101]
	v_exp_f32_e32 v233, v233
	v_rcp_f32_e32 v230, v230
	v_add_f32_e32 v232, 1.0, v232
	v_mfma_f32_16x16x32_f16 v[214:217], v[74:77], v[150:153], v[102:105]
	v_fma_f32 v235, v233, s41, s41
	v_fma_f32 v236, -v228, v230, v230
	v_rcp_f32_e32 v232, v232
	v_fma_f32 v235, v231, v235, v235
	v_fma_f32 v198, v198, v227, v236
	v_rcp_f32_e32 v235, v235
	s_nop 0
	v_fma_f32 v231, -v233, v235, v235
	v_exp_f32_e32 v236, v198
	v_fma_f32 v199, v199, v232, v231
	v_exp_f32_e32 v231, v199
	v_add_f32_e32 v227, 1.0, v236
	v_add_f32_e32 v232, 1.0, v231
	v_fma_f32 v232, v234, v232, v232
	v_fma_f32 v227, v229, v227, v227
	v_rcp_f32_e32 v232, v232
	s_nop 0
	v_fma_f32 v231, -v231, v232, v232
	v_rcp_f32_e32 v227, v227
	s_nop 0
	v_fma_f32 v236, -v236, v227, v227
	v_cvt_pk_f16_f32 v247, v236, v231
	ds_write_b64 v206, v[246:247] offset:12288
	v_mfma_f32_16x16x32_f16 v[210:213], v[66:69], v[154:157], v[210:213]
	v_mfma_f32_16x16x32_f16 v[214:217], v[78:81], v[154:157], v[214:217]
	v_mov_b32_e32 v205, v246
	v_mov_b32_e32 v207, v247
	buffer_load_dwordx2 v[194:195], v209, s[20:23], s45 offen
	s_add_i32 s40, s40, 1
	s_add_i32 s44, s44, 0x1000
	s_waitcnt lgkmcnt(0)
	s_barrier
	v_add_u32_e32 v250, 0x1000, v206
	v_add_u32_e32 v248, 0x1000, v252
	v_add_u32_e32 v249, 0x1000, v253
	s_mov_b32 s45, 0xc00000
	s_mov_b32 s46, 0x30000
